# speedup vs baseline: 1.0318x; 1.0318x over previous
_Z11k1_temporalPKfS0_S0_PKDF16_S0_S0_S0_S0_Pf:
	s_lshr_b32 s26, s2, 3
	v_readfirstlane_b32 s12, v0
	s_mul_hi_u32 s3, s12, 0xaaaaaaab
	s_lshr_b32 s22, s3, 7
	s_lshl_b32 s2, s2, 1
	s_add_i32 s2, s22, s2
	s_lshr_b32 s13, s12, 6
	s_ashr_i32 s6, s2, 31
	s_mul_hi_u32 s3, s13, 0x55555556
	s_lshr_b32 s6, s6, 25
	s_mul_i32 s3, s3, 3
	s_add_i32 s6, s2, s6
	s_load_dwordx2 s[4:5], s[0:1], 0x0
	s_sub_i32 s3, s13, s3
	v_and_b32_e32 v8, 31, v0
	s_lshr_b32 s7, s6, 7
	s_and_b32 s6, s6, 0xffffff80
	v_lshl_or_b32 v9, s3, 5, v8
	s_mulk_i32 s7, 0x60
	s_sub_i32 s2, s2, s6
	v_add_u32_e32 v1, s7, v9
	v_lshl_add_u32 v64, v1, 7, s2
	v_ashrrev_i32_e32 v65, 31, v64
	s_waitcnt lgkmcnt(0)
	v_lshl_add_u64 v[2:3], v[64:65], 2, s[4:5]
	global_load_dword v18, v[2:3], off
	s_load_dwordx8 s[4:11], s[0:1], 0x20
	v_cmp_lt_u32_e32 vcc, 63, v0
	s_and_saveexec_b64 s[2:3], vcc
	s_xor_b64 s[2:3], exec, s[2:3]
	s_cbranch_execz .LBB1_18
	s_movk_i32 s14, 0x7f
	v_cmp_lt_u32_e32 vcc, s14, v0
	s_and_saveexec_b64 s[14:15], vcc
	s_xor_b64 s[14:15], exec, s[14:15]
	s_cbranch_execz .LBB1_15
	s_movk_i32 s16, 0x1cf
	v_cmp_lt_u32_e32 vcc, s16, v0
	s_and_saveexec_b64 s[16:17], vcc
	s_xor_b64 s[16:17], exec, s[16:17]
	s_cbranch_execz .LBB1_12
	s_movk_i32 s18, 0x2cf
	v_cmp_lt_u32_e32 vcc, s18, v0
	s_and_saveexec_b64 s[18:19], vcc
	s_xor_b64 s[18:19], exec, s[18:19]
	s_cbranch_execz .LBB1_9
	s_movk_i32 s20, 0x30f
	v_cmp_lt_u32_e32 vcc, s20, v0
	v_mov_b32_e32 v3, 0
	s_and_saveexec_b64 s[20:21], vcc
	s_xor_b64 s[20:21], exec, s[20:21]
	s_cbranch_execz .LBB1_6
	v_lshlrev_b32_e32 v2, 2, v0
	s_movk_i32 s24, 0xf3c0
	s_waitcnt lgkmcnt(0)
	v_lshl_add_u64 v[2:3], s[10:11], 0, v[2:3]
	s_mov_b32 s25, -1
	v_lshl_add_u64 v[4:5], v[2:3], 0, s[24:25]

.LBB1_32:
	s_or_b64 exec, exec, s[4:5]
	v_lshl_add_u32 v2, v0, 2, 0
	s_movk_i32 s2, 0x290
	v_add_u32_e32 v2, 0x10000, v2
	v_cmp_gt_u32_e32 vcc, s2, v0
	s_waitcnt vmcnt(0)
	ds_write_b32 v2, v1
	s_and_saveexec_b64 s[2:3], vcc
	ds_write_b32 v2, v10 offset:1536
	s_or_b64 exec, exec, s[2:3]
	s_movk_i32 s2, 0x110
	v_cmp_gt_u32_e32 vcc, s2, v0
	s_and_saveexec_b64 s[2:3], vcc
	ds_write_b32 v2, v3 offset:3072
	s_or_b64 exec, exec, s[2:3]
	s_mulk_i32 s22, 0x180
	v_and_b32_e32 v1, 63, v0
	s_add_i32 s4, s22, 0
	s_add_i32 s4, s4, 0x11040
	v_cmp_gt_u32_e32 vcc, 32, v1
	s_and_saveexec_b64 s[2:3], vcc
	v_lshl_add_u32 v2, v9, 2, s4
	ds_write_b32 v2, v18
	s_or_b64 exec, exec, s[2:3]
	s_cmpk_gt_u32 s12, 0xfff
	s_waitcnt lgkmcnt(0)
	s_barrier
	s_cbranch_scc1 .LBB1_41
	s_load_dwordx2 s[2:3], s[0:1], 0x18
	s_add_i32 s5, s13, -6
	s_lshl_b32 s27, s26, 1
	s_mov_b32 s7, 0
	v_lshlrev_b32_e32 v4, 4, v1
	v_mov_b32_e32 v5, 0
	s_waitcnt lgkmcnt(0)
	s_add_u32 s2, s2, 0x8000
	s_addc_u32 s3, s3, 0
	v_lshl_add_u64 v[4:5], s[2:3], 0, v[4:5]
.Lmy_k1dma:
	s_add_i32 s5, s5, 6
	s_add_i32 s6, s5, s27
	s_and_b32 s6, s6, 63
	s_lshl_b32 s6, s6, 10
	s_mov_b32 m0, s6
	v_lshl_add_u64 v[2:3], v[4:5], 0, s[6:7]
	global_load_lds_dwordx4 v[2:3], off
	s_cmp_lt_u32 s5, 58
	s_cbranch_scc1 .Lmy_k1dma

	.amdhsa_kernel _Z11k1_temporalPKfS0_S0_PKDF16_S0_S0_S0_S0_Pf
		.amdhsa_group_segment_fixed_size 0
		.amdhsa_private_segment_fixed_size 0
		.amdhsa_kernarg_size 72
		.amdhsa_user_sgpr_count 2
		.amdhsa_user_sgpr_dispatch_ptr 0
		.amdhsa_user_sgpr_queue_ptr 0
		.amdhsa_user_sgpr_kernarg_segment_ptr 1
		.amdhsa_user_sgpr_dispatch_id 0
		.amdhsa_user_sgpr_kernarg_preload_length 0
		.amdhsa_user_sgpr_kernarg_preload_offset 0
		.amdhsa_user_sgpr_private_segment_size 0
		.amdhsa_uses_dynamic_stack 0
		.amdhsa_enable_private_segment 0
		.amdhsa_system_sgpr_workgroup_id_x 1
		.amdhsa_system_sgpr_workgroup_id_y 0
		.amdhsa_system_sgpr_workgroup_id_z 0
		.amdhsa_system_sgpr_workgroup_info 0
		.amdhsa_system_vgpr_workitem_id 0
		.amdhsa_next_free_vgpr 247
		.amdhsa_next_free_sgpr 28
		.amdhsa_accum_offset 248
		.amdhsa_reserve_vcc 1
		.amdhsa_float_round_mode_32 0
		.amdhsa_float_round_mode_16_64 0
		.amdhsa_float_denorm_mode_32 3
		.amdhsa_float_denorm_mode_16_64 3
		.amdhsa_dx10_clamp 1
		.amdhsa_ieee_mode 1
		.amdhsa_fp16_overflow 0
		.amdhsa_tg_split 0
		.amdhsa_exception_fp_ieee_invalid_op 0
		.amdhsa_exception_fp_denorm_src 0
		.amdhsa_exception_fp_ieee_div_zero 0
		.amdhsa_exception_fp_ieee_overflow 0
		.amdhsa_exception_fp_ieee_underflow 0
		.amdhsa_exception_fp_ieee_inexact 0
		.amdhsa_exception_int_div_zero 0
	.end_amdhsa_kernel

.LBB2_79:
	v_lshrrev_b32_e32 v2, 2, v0
	v_and_b32_e32 v3, 3, v0
	s_add_i32 s21, 0, 0x16000
	v_mul_u32_u24_e32 v2, 0x90, v2
	v_lshlrev_b32_e32 v160, 2, v3
	v_add3_u32 v2, s21, v2, v160
	v_add_u32_e32 v2, 0x80, v2
	s_waitcnt vmcnt(11)
	ds_write2st64_b32 v2, v8, v9 offset1:72
	v_lshl_add_u32 v125, v4, 1, 0
	s_waitcnt vmcnt(8)
	s_waitcnt lgkmcnt(0)
	s_barrier
	ds_read_b128 v[2:5], v125
	ds_read_b128 v[18:21], v125 offset:1024
	s_waitcnt lgkmcnt(1)
	v_mfma_f32_32x32x16_f16 v[2:17], v[2:5], v[110:113], 0
	v_mul_u32_u24_e32 v165, 0x48, v164
	v_lshl_add_u32 v173, v165, 1, s21
	s_mul_i32 s18, s28, 0x4800
	s_add_i32 s18, s21, s18
	s_movk_i32 s23, 0x90
	v_lshlrev_b32_e32 v69, 4, v164
	s_mul_i32 s20, s28, 0x4400
	s_waitcnt lgkmcnt(0)
	v_mfma_f32_32x32x16_f16 v[2:17], v[18:21], v[106:109], v[2:17]
	ds_read_b128 v[18:21], v125 offset:2048
	ds_read_b128 v[22:25], v125 offset:3072
	ds_read_b128 v[34:37], v125 offset:9216
	ds_read_b128 v[38:41], v125 offset:10240
	s_add_i32 s20, s20, 0
	s_add_i32 s20, s20, 0x1f000
	s_lshl_b32 s15, s15, 1
	s_add_i32 s15, s20, s15
	s_waitcnt lgkmcnt(3)
	v_mfma_f32_32x32x16_f16 v[2:17], v[18:21], v[102:105], v[2:17]
	ds_read_b128 v[18:21], v125 offset:8192
	ds_read_b128 v[72:75], v125 offset:4096
	ds_read_b128 v[76:79], v125 offset:5120
	v_add_u32_e32 v167, s15, v69
	s_movk_i32 s15, 0x110
	s_load_dwordx8 s[4:11], s[0:1], 0x88
	v_lshlrev_b32_e32 v126, 2, v164
	s_mov_b32 s19, 0
	s_waitcnt lgkmcnt(0)
	v_mfma_f32_32x32x16_f16 v[2:17], v[22:25], v[98:101], v[2:17]
	s_and_b64 vcc, exec, s[2:3]
	v_mfma_f32_32x32x16_f16 v[18:33], v[18:21], v[110:113], 0
	v_mfma_f32_32x32x16_f16 v[18:33], v[34:37], v[106:109], v[18:33]
	ds_read_b128 v[80:83], v173 offset:128
	ds_read_b128 v[34:37], v125 offset:11264
	ds_read_b128 v[84:87], v125 offset:6144
	ds_read_b128 v[88:91], v125 offset:7168
	ds_read_b128 v[92:95], v173 offset:416
	s_waitcnt lgkmcnt(4)
	s_nop 2
	v_fmamk_f32 v68, v80, 0x3eb8aa3b, v2
	v_fmamk_f32 v70, v81, 0x3eb8aa3b, v3
	v_fmamk_f32 v4, v82, 0x3eb8aa3b, v4
	v_mfma_f32_32x32x16_f16 v[18:33], v[38:41], v[102:105], v[18:33]
	ds_read_b128 v[114:117], v173 offset:704
	ds_read_b128 v[128:131], v173 offset:992
	ds_read_b128 v[38:41], v125 offset:12288
	ds_read_b128 v[62:65], v173 offset:1280
	ds_read_b128 v[58:61], v173 offset:1568
	ds_read_b128 v[54:57], v173 offset:1856
	ds_read_b128 v[50:53], v173 offset:2144
	ds_read_b128 v[132:135], v125 offset:13312
	ds_read_b128 v[136:139], v173 offset:2432
	ds_read_b128 v[140:143], v125 offset:14336
	ds_read_b128 v[144:147], v125 offset:15360
	ds_read_b128 v[148:151], v173 offset:2720
	v_fmamk_f32 v5, v83, 0x3eb8aa3b, v5
	s_waitcnt lgkmcnt(12)
	v_fmamk_f32 v6, v92, 0x3eb8aa3b, v6
	v_fmamk_f32 v7, v93, 0x3eb8aa3b, v7
	v_fmamk_f32 v8, v94, 0x3eb8aa3b, v8
	v_mfma_f32_32x32x16_f16 v[18:33], v[34:37], v[98:101], v[18:33]
	v_fmamk_f32 v9, v95, 0x3eb8aa3b, v9
	s_waitcnt lgkmcnt(11)
	v_fmamk_f32 v10, v114, 0x3eb8aa3b, v10
	v_fmamk_f32 v11, v115, 0x3eb8aa3b, v11
	v_fmamk_f32 v12, v116, 0x3eb8aa3b, v12
	v_fmamk_f32 v13, v117, 0x3eb8aa3b, v13
	s_waitcnt lgkmcnt(10)
	v_fmamk_f32 v14, v128, 0x3eb8aa3b, v14
	v_fmamk_f32 v15, v129, 0x3eb8aa3b, v15
	s_waitcnt lgkmcnt(9)
	v_mfma_f32_32x32x16_f16 v[34:49], v[38:41], v[110:113], 0
	s_waitcnt lgkmcnt(3)
	v_add_f32_e32 v2, v18, v136
	v_add_f32_e32 v3, v19, v137
	v_add_f32_e32 v71, v20, v138
	v_add_f32_e32 v80, v21, v139
	ds_read_b128 v[18:21], v173 offset:3008
	s_waitcnt lgkmcnt(1)
	v_add_f32_e32 v81, v22, v148
	v_add_f32_e32 v96, v23, v149
	v_mfma_f32_32x32x16_f16 v[34:49], v[132:135], v[106:109], v[34:49]
	v_add_f32_e32 v97, v24, v150
	v_add_f32_e32 v122, v25, v151
	ds_read_b128 v[22:25], v173 offset:3296
	s_waitcnt lgkmcnt(1)
	v_add_f32_e32 v123, v26, v18
	v_add_f32_e32 v127, v27, v19
	v_add_f32_e32 v132, v28, v20
	v_add_f32_e32 v133, v29, v21
	v_mfma_f32_32x32x16_f16 v[34:49], v[140:143], v[102:105], v[34:49]
	s_waitcnt lgkmcnt(0)
	v_add_f32_e32 v134, v30, v22
	v_add_f32_e32 v135, v31, v23
	v_add_f32_e32 v136, v32, v24
	v_add_f32_e32 v137, v33, v25
	ds_read_b128 v[18:21], v173 offset:3584
	ds_read_b128 v[22:25], v173 offset:3872
	v_fmamk_f32 v16, v130, 0x3eb8aa3b, v16
	v_fmac_f32_e32 v17, 0x3eb8aa3b, v131
	v_mfma_f32_32x32x16_f16 v[34:49], v[144:147], v[98:101], v[34:49]
	s_waitcnt lgkmcnt(1)
	s_nop 10
	v_add_f32_e32 v138, v34, v18
	v_add_f32_e32 v139, v35, v19
	v_add_f32_e32 v140, v36, v20
	v_add_f32_e32 v141, v37, v21
	s_waitcnt lgkmcnt(0)
	v_add_f32_e32 v38, v38, v22
	ds_read_b128 v[18:21], v173 offset:4160
	v_add_f32_e32 v39, v39, v23
	v_add_f32_e32 v40, v40, v24
	v_add_f32_e32 v41, v41, v25
	ds_read_b128 v[22:25], v173 offset:4448
	v_mov_b32_e32 v34, s18
	v_mad_u32_u24 v34, v1, s23, v34
	v_add_u32_e32 v166, v34, v69
	v_cvt_pkrtz_f16_f32 v34, v2, v3
	v_cvt_pkrtz_f16_f32 v35, v71, v80
	v_cvt_pkrtz_f16_f32 v36, v81, v96
	v_cvt_pkrtz_f16_f32 v37, v97, v122
	ds_write_b128 v166, v[34:37]
	v_cvt_pkrtz_f16_f32 v34, v123, v127
	v_cvt_pkrtz_f16_f32 v35, v132, v133
	v_cvt_pkrtz_f16_f32 v36, v134, v135
	v_cvt_pkrtz_f16_f32 v37, v136, v137
	s_waitcnt lgkmcnt(2)
	v_add_f32_e32 v42, v42, v18
	v_add_f32_e32 v43, v43, v19
	v_add_f32_e32 v44, v44, v20
	v_add_f32_e32 v45, v45, v21
	s_waitcnt lgkmcnt(1)
	v_add_f32_e32 v46, v46, v22
	v_add_f32_e32 v47, v47, v23
	v_add_f32_e32 v48, v48, v24
	v_add_f32_e32 v49, v49, v25
	ds_write_b128 v166, v[34:37] offset:32
	v_cvt_pkrtz_f16_f32 v34, v138, v139
	v_cvt_pkrtz_f16_f32 v35, v140, v141
	v_cvt_pkrtz_f16_f32 v36, v38, v39
	v_cvt_pkrtz_f16_f32 v37, v40, v41
	ds_write_b128 v166, v[34:37] offset:64
	v_cvt_pkrtz_f16_f32 v34, v42, v43
	v_cvt_pkrtz_f16_f32 v35, v44, v45
	v_cvt_pkrtz_f16_f32 v36, v46, v47
	v_cvt_pkrtz_f16_f32 v37, v48, v49
	ds_write_b128 v166, v[34:37] offset:96
	ds_read_b128 v[34:37], v125 offset:16384
	v_lshrrev_b32_e32 v2, 2, v174
	v_mul_u32_u24_e32 v2, 0x48, v2
	v_lshlrev_b32_e32 v168, 1, v2
	v_add3_u32 v2, s21, v168, v160
	v_mfma_f32_32x32x16_f16 v[18:33], v[72:75], v[110:113], 0
	ds_read_b32 v2, v2 offset:4736
	ds_read_b128 v[72:75], v125 offset:17408
	v_mad_u32_u24 v71, v174, s15, v167
	s_waitcnt lgkmcnt(2)
	v_mfma_f32_32x32x16_f16 v[34:49], v[110:113], v[34:37], 0
	v_mfma_f32_32x32x16_f16 v[18:33], v[76:79], v[106:109], v[18:33]
	ds_read_b128 v[76:79], v125 offset:19456
	s_waitcnt lgkmcnt(1)
	v_mfma_f32_32x32x16_f16 v[34:49], v[106:109], v[72:75], v[34:49]
	ds_read_b128 v[72:75], v125 offset:18432
	s_waitcnt lgkmcnt(0)
	v_mfma_f32_32x32x16_f16 v[34:49], v[102:105], v[72:75], v[34:49]
	v_mfma_f32_32x32x16_f16 v[34:49], v[98:101], v[76:79], v[34:49]
	v_mfma_f32_32x32x16_f16 v[18:33], v[84:87], v[102:105], v[18:33]
	s_nop 10
	v_add_f32_e32 v3, v2, v34
	v_add_f32_e32 v34, v2, v35
	v_add_f32_e32 v35, v2, v36
	v_add_f32_e32 v36, v2, v37
	v_add_f32_e32 v37, v2, v38
	v_add_f32_e32 v38, v2, v39
	v_add_f32_e32 v39, v2, v40
	v_add_f32_e32 v40, v2, v41
	v_add_f32_e32 v41, v2, v42
	v_add_f32_e32 v42, v2, v43
	v_add_f32_e32 v43, v2, v44
	v_add_f32_e32 v44, v2, v45
	v_add_f32_e32 v45, v2, v46
	v_add_f32_e32 v46, v2, v47
	v_add_f32_e32 v47, v2, v48
	v_add_f32_e32 v2, v2, v49
	v_cvt_pkrtz_f16_f32 v34, v3, v34
	v_cvt_pkrtz_f16_f32 v35, v35, v36
	v_cvt_pkrtz_f16_f32 v36, v37, v38
	v_cvt_pkrtz_f16_f32 v37, v39, v40
	ds_write_b128 v71, v[34:37]
	v_cvt_pkrtz_f16_f32 v34, v41, v42
	v_cvt_pkrtz_f16_f32 v35, v43, v44
	v_cvt_pkrtz_f16_f32 v36, v45, v46
	v_cvt_pkrtz_f16_f32 v37, v47, v2
	ds_write_b128 v71, v[34:37] offset:32
	ds_read_b128 v[34:37], v125 offset:20480
	v_or_b32_e32 v2, 32, v174
	v_lshrrev_b32_e32 v2, 2, v2
	v_mul_u32_u24_e32 v2, 0x48, v2
	v_lshlrev_b32_e32 v169, 1, v2
	v_add3_u32 v2, s21, v169, v160
	v_mfma_f32_32x32x16_f16 v[18:33], v[88:91], v[98:101], v[18:33]
	ds_read_b32 v2, v2 offset:4736
	ds_read_b128 v[72:75], v125 offset:21504
	s_waitcnt lgkmcnt(2)
	v_mfma_f32_32x32x16_f16 v[34:49], v[110:113], v[34:37], 0
	s_nop 7
	v_fmamk_f32 v26, v54, 0x3eb8aa3b, v26
	v_fmamk_f32 v27, v55, 0x3eb8aa3b, v27
	v_fmamk_f32 v28, v56, 0x3eb8aa3b, v28
	v_fmamk_f32 v29, v57, 0x3eb8aa3b, v29
	ds_read_b128 v[54:57], v125 offset:22528
	v_fmamk_f32 v22, v58, 0x3eb8aa3b, v22
	v_fmamk_f32 v23, v59, 0x3eb8aa3b, v23
	s_waitcnt lgkmcnt(1)
	v_mfma_f32_32x32x16_f16 v[34:49], v[106:109], v[72:75], v[34:49]
	v_fmamk_f32 v24, v60, 0x3eb8aa3b, v24
	v_fmamk_f32 v25, v61, 0x3eb8aa3b, v25
	ds_read_b128 v[58:61], v125 offset:23552
	v_fmamk_f32 v18, v62, 0x3eb8aa3b, v18
	v_fmamk_f32 v19, v63, 0x3eb8aa3b, v19
	v_fmamk_f32 v20, v64, 0x3eb8aa3b, v20
	v_fmamk_f32 v21, v65, 0x3eb8aa3b, v21
	s_waitcnt lgkmcnt(1)
	v_mfma_f32_32x32x16_f16 v[34:49], v[102:105], v[54:57], v[34:49]
	v_fmamk_f32 v30, v50, 0x3eb8aa3b, v30
	v_fmamk_f32 v31, v51, 0x3eb8aa3b, v31
	v_fmamk_f32 v32, v52, 0x3eb8aa3b, v32
	v_fmac_f32_e32 v33, 0x3eb8aa3b, v53
	s_waitcnt lgkmcnt(0)
	v_mfma_f32_32x32x16_f16 v[34:49], v[98:101], v[58:61], v[34:49]
	s_nop 11
	v_add_f32_e32 v3, v2, v34
	v_add_f32_e32 v34, v2, v35
	v_add_f32_e32 v35, v2, v36
	v_add_f32_e32 v36, v2, v37
	v_add_f32_e32 v37, v2, v38
	v_add_f32_e32 v38, v2, v39
	v_add_f32_e32 v39, v2, v40
	v_add_f32_e32 v40, v2, v41
	v_add_f32_e32 v41, v2, v42
	v_add_f32_e32 v42, v2, v43
	v_add_f32_e32 v43, v2, v44
	v_add_f32_e32 v44, v2, v45
	v_add_f32_e32 v45, v2, v46
	v_add_f32_e32 v46, v2, v47
	v_add_f32_e32 v47, v2, v48
	v_add_f32_e32 v2, v2, v49
	v_cvt_pkrtz_f16_f32 v34, v3, v34
	v_cvt_pkrtz_f16_f32 v35, v35, v36
	v_cvt_pkrtz_f16_f32 v36, v37, v38
	v_cvt_pkrtz_f16_f32 v37, v39, v40
	ds_write_b128 v71, v[34:37] offset:8704
	v_cvt_pkrtz_f16_f32 v34, v41, v42
	v_cvt_pkrtz_f16_f32 v35, v43, v44
	v_cvt_pkrtz_f16_f32 v36, v45, v46
	v_cvt_pkrtz_f16_f32 v37, v47, v2
	ds_write_b128 v71, v[34:37] offset:8736
	s_waitcnt vmcnt(0) lgkmcnt(0)
	s_barrier
	s_cbranch_vccz .LBB2_82
	s_lshl_b32 s2, s22, 10
	s_add_i32 s23, s2, 0
	s_lshl_b64 s[2:3], s[14:15], 4
	s_add_i32 s21, s22, -8
	s_and_b32 s3, s3, 15
	s_and_b32 s2, s2, 0xfffffc00
	s_add_u32 s2, s16, s2
	s_addc_u32 s3, s17, s3
	v_lshl_add_u64 v[2:3], v[120:121], 1, s[2:3]
	s_mov_b64 s[2:3], 0x30000
	v_lshl_add_u64 v[2:3], v[2:3], 0, s[2:3]
	s_mov_b64 s[2:3], 0x2000

.LBB2_83:
	s_lshl_b32 s30, s18, 11
	s_mov_b32 s31, 0
	v_lshl_add_u64 v[252:253], v[122:123], 0, s[30:31]
	s_bitset1_b32 s30, 12
	v_lshl_add_u64 v[254:255], v[122:123], 0, s[30:31]
	global_load_dwordx4 v[240:243], v[254:255], off
	global_load_dwordx4 v[236:239], v[252:253], off
	global_load_dwordx4 v[244:247], v[252:253], off offset:1024
	global_load_dwordx4 v[248:251], v[254:255], off offset:1024
	s_lshl_b32 s24, s18, 6
	v_add3_u32 v184, v171, s24, v172
	ds_read_b128 v[38:41], v184
	ds_read_b128 v[42:45], v184 offset:4608
	v_lshl_or_b32 v183, s18, 5, v174
	v_mad_u32_u24 v183, v183, s15, v163
	s_waitcnt lgkmcnt(0)
	v_mfma_f32_32x32x16_f16 v[82:97], v[38:41], v[34:37], 0
	ds_read_b128 v[38:41], v184 offset:9216
	v_mfma_f32_32x32x16_f16 v[66:81], v[42:45], v[34:37], 0
	s_nop 9
	ds_read_b128 v[42:45], v184 offset:13824
	s_waitcnt lgkmcnt(0)
	v_mfma_f32_32x32x16_f16 v[50:65], v[38:41], v[34:37], 0
	v_mfma_f32_32x32x16_f16 v[34:49], v[42:45], v[34:37], 0
	s_nop 3
	s_nop 1
	v_exp_f32_e32 v66, v66
	v_exp_f32_e32 v67, v67
	v_exp_f32_e32 v68, v68
	v_exp_f32_e32 v69, v69
	v_cvt_pkrtz_f16_f32 v66, v66, v67
	v_cvt_pkrtz_f16_f32 v67, v68, v69
	v_exp_f32_e32 v68, v70
	v_exp_f32_e32 v69, v71
	v_exp_f32_e32 v70, v72
	v_exp_f32_e32 v71, v73
	v_cvt_pkrtz_f16_f32 v68, v68, v69
	v_cvt_pkrtz_f16_f32 v69, v70, v71
	v_exp_f32_e32 v70, v74
	v_exp_f32_e32 v71, v75
	v_exp_f32_e32 v72, v76
	v_exp_f32_e32 v73, v77
	v_cvt_pkrtz_f16_f32 v70, v70, v71
	v_cvt_pkrtz_f16_f32 v71, v72, v73
	v_exp_f32_e32 v50, v50
	v_exp_f32_e32 v51, v51
	v_exp_f32_e32 v72, v78
	v_exp_f32_e32 v73, v79
	v_exp_f32_e32 v74, v80
	v_exp_f32_e32 v75, v81
	v_exp_f32_e32 v52, v52
	v_exp_f32_e32 v53, v53
	v_cvt_pkrtz_f16_f32 v50, v50, v51
	v_cvt_pkrtz_f16_f32 v72, v72, v73
	v_cvt_pkrtz_f16_f32 v73, v74, v75
	v_and_b32_e32 v74, v143, v50
	v_cvt_pkrtz_f16_f32 v50, v52, v53
	v_and_b32_e32 v75, v144, v50
	v_exp_f32_e32 v50, v54
	v_exp_f32_e32 v51, v55
	v_exp_f32_e32 v52, v56
	v_exp_f32_e32 v53, v57
	v_cvt_pkrtz_f16_f32 v50, v50, v51
	v_and_b32_e32 v76, v145, v50
	v_cvt_pkrtz_f16_f32 v50, v52, v53
	v_and_b32_e32 v77, v146, v50
	v_exp_f32_e32 v50, v58
	v_exp_f32_e32 v51, v59
	v_exp_f32_e32 v52, v60
	v_exp_f32_e32 v53, v61
	v_exp_f32_e32 v82, v82
	v_exp_f32_e32 v83, v83
	v_exp_f32_e32 v84, v84
	v_exp_f32_e32 v85, v85
	v_cvt_pkrtz_f16_f32 v50, v50, v51
	v_and_b32_e32 v78, v147, v50
	v_cvt_pkrtz_f16_f32 v50, v52, v53
	v_cvt_pkrtz_f16_f32 v82, v82, v83
	v_cvt_pkrtz_f16_f32 v83, v84, v85
	v_exp_f32_e32 v84, v86
	v_exp_f32_e32 v85, v87
	v_and_b32_e32 v79, v148, v50
	v_exp_f32_e32 v86, v88
	v_exp_f32_e32 v87, v89
	v_exp_f32_e32 v50, v62
	v_exp_f32_e32 v51, v63
	v_exp_f32_e32 v52, v64
	v_exp_f32_e32 v53, v65
	v_cvt_pkrtz_f16_f32 v84, v84, v85
	v_cvt_pkrtz_f16_f32 v85, v86, v87
	v_cvt_pkrtz_f16_f32 v50, v50, v51
	v_exp_f32_e32 v86, v90
	v_exp_f32_e32 v87, v91
	v_exp_f32_e32 v88, v92
	v_exp_f32_e32 v89, v93
	v_and_b32_e32 v80, v149, v50
	v_cvt_pkrtz_f16_f32 v50, v52, v53
	v_and_b32_e32 v81, v150, v50
	ds_read_b128 v[50:53], v183
	v_cvt_pkrtz_f16_f32 v86, v86, v87
	v_cvt_pkrtz_f16_f32 v87, v88, v89
	v_exp_f32_e32 v88, v94
	v_exp_f32_e32 v89, v95
	v_exp_f32_e32 v90, v96
	v_exp_f32_e32 v91, v97
	v_exp_f32_e32 v34, v34
	v_exp_f32_e32 v35, v35
	v_exp_f32_e32 v36, v36
	v_exp_f32_e32 v37, v37
	v_and_b32_e32 v82, v127, v82
	v_and_b32_e32 v83, v128, v83
	v_and_b32_e32 v84, v129, v84
	v_and_b32_e32 v85, v130, v85
	v_cvt_pkrtz_f16_f32 v88, v88, v89
	v_cvt_pkrtz_f16_f32 v89, v90, v91
	ds_read_b128 v[90:93], v183 offset:32
	s_waitcnt lgkmcnt(0)
	v_mfma_f32_32x32x16_f16 v[50:65], v[50:53], v[82:85], 0
	v_cvt_pkrtz_f16_f32 v34, v34, v35
	v_cvt_pkrtz_f16_f32 v35, v36, v37
	v_exp_f32_e32 v36, v38
	v_exp_f32_e32 v37, v39
	v_exp_f32_e32 v38, v40
	v_exp_f32_e32 v39, v41
	v_and_b32_e32 v86, v131, v86
	v_and_b32_e32 v87, v132, v87
	v_and_b32_e32 v88, v133, v88
	v_and_b32_e32 v89, v134, v89
	v_cvt_pkrtz_f16_f32 v36, v36, v37
	v_cvt_pkrtz_f16_f32 v37, v38, v39
	ds_read_b128 v[38:41], v183 offset:64
	v_mfma_f32_32x32x16_f16 v[50:65], v[90:93], v[86:89], v[50:65]
	v_mov_b32_e32 v186, 0
	v_dot2c_f32_f16_e32 v186, 0x3c003c00, v82
	v_dot2c_f32_f16_e32 v186, 0x3c003c00, v83
	v_dot2c_f32_f16_e32 v186, 0x3c003c00, v84
	v_dot2c_f32_f16_e32 v186, 0x3c003c00, v85
	v_and_b32_e32 v66, v135, v66
	v_and_b32_e32 v67, v136, v67
	v_and_b32_e32 v68, v137, v68
	v_and_b32_e32 v69, v138, v69
	ds_read_b128 v[82:85], v183 offset:96
	s_waitcnt lgkmcnt(0)
	v_mfma_f32_32x32x16_f16 v[50:65], v[38:41], v[66:69], v[50:65]
	v_exp_f32_e32 v42, v42
	v_exp_f32_e32 v43, v43
	v_and_b32_e32 v70, v139, v70
	v_and_b32_e32 v71, v140, v71
	v_and_b32_e32 v72, v141, v72
	v_and_b32_e32 v73, v142, v73
	v_cvt_pkrtz_f16_f32 v38, v42, v43
	v_exp_f32_e32 v39, v44
	v_exp_f32_e32 v44, v45
	ds_read_b128 v[40:43], v183 offset:128
	v_dot2c_f32_f16_e32 v186, 0x3c003c00, v86
	v_mfma_f32_32x32x16_f16 v[50:65], v[82:85], v[70:73], v[50:65]
	v_dot2c_f32_f16_e32 v186, 0x3c003c00, v87
	v_dot2c_f32_f16_e32 v186, 0x3c003c00, v88
	v_dot2c_f32_f16_e32 v186, 0x3c003c00, v89
	v_dot2c_f32_f16_e32 v186, 0x3c003c00, v66
	v_dot2c_f32_f16_e32 v186, 0x3c003c00, v67
	v_dot2c_f32_f16_e32 v186, 0x3c003c00, v68
	v_dot2c_f32_f16_e32 v186, 0x3c003c00, v69
	ds_read_b128 v[66:69], v183 offset:160
	s_waitcnt lgkmcnt(0)
	v_mfma_f32_32x32x16_f16 v[50:65], v[40:43], v[74:77], v[50:65]
	v_dot2c_f32_f16_e32 v186, 0x3c003c00, v70
	v_dot2c_f32_f16_e32 v186, 0x3c003c00, v71
	v_dot2c_f32_f16_e32 v186, 0x3c003c00, v72
	v_cvt_pkrtz_f16_f32 v39, v39, v44
	v_dot2c_f32_f16_e32 v186, 0x3c003c00, v73
	v_exp_f32_e32 v46, v46
	v_exp_f32_e32 v40, v47
	v_exp_f32_e32 v47, v49
	ds_read_b128 v[42:45], v183 offset:192
	v_dot2c_f32_f16_e32 v186, 0x3c003c00, v74
	v_mfma_f32_32x32x16_f16 v[50:65], v[66:69], v[78:81], v[50:65]
	v_dot2c_f32_f16_e32 v186, 0x3c003c00, v75
	v_dot2c_f32_f16_e32 v186, 0x3c003c00, v76
	v_dot2c_f32_f16_e32 v186, 0x3c003c00, v77
	v_exp_f32_e32 v41, v48
	v_dot2c_f32_f16_e32 v186, 0x3c003c00, v78
	v_dot2c_f32_f16_e32 v186, 0x3c003c00, v79
	v_dot2c_f32_f16_e32 v186, 0x3c003c00, v80
	v_dot2c_f32_f16_e32 v186, 0x3c003c00, v81
	v_and_b32_e32 v34, v151, v34
	v_and_b32_e32 v35, v152, v35
	v_and_b32_e32 v36, v153, v36
	v_and_b32_e32 v37, v154, v37
	v_cvt_pkrtz_f16_f32 v40, v46, v40
	v_cvt_pkrtz_f16_f32 v41, v41, v47
	ds_read_b128 v[46:49], v183 offset:224
	v_dot2c_f32_f16_e32 v186, 0x3c003c00, v34
	s_waitcnt lgkmcnt(0)
	v_mfma_f32_32x32x16_f16 v[50:65], v[42:45], v[34:37], v[50:65]
	v_dot2c_f32_f16_e32 v186, 0x3c003c00, v35
	v_dot2c_f32_f16_e32 v186, 0x3c003c00, v36
	v_dot2c_f32_f16_e32 v186, 0x3c003c00, v37
	v_and_b32_e32 v38, v155, v38
	v_dot2c_f32_f16_e32 v186, 0x3c003c00, v38
	v_and_b32_e32 v39, v156, v39
	v_dot2c_f32_f16_e32 v186, 0x3c003c00, v39
	v_and_b32_e32 v40, v157, v40
	v_dot2c_f32_f16_e32 v186, 0x3c003c00, v40
	v_and_b32_e32 v41, v158, v41
	v_dot2c_f32_f16_e32 v186, 0x3c003c00, v41
	s_nop 0
	v_mfma_f32_32x32x16_f16 v[50:65], v[46:49], v[38:41], v[50:65]
	s_nop 0
	v_mov_b32_e32 v34, v186
	v_mov_b32_e32 v35, v186
	s_nop 1
	v_permlane32_swap_b32_e32 v34, v35
	v_cndmask_b32_e64 v34, v34, v35, s[2:3]
	v_add_f32_e32 v34, v186, v34
	v_rcp_f32_e32 v34, v34
	s_nop 2
	v_mul_f32_e32 v185, v34, v50
	v_mul_f32_e32 v186, v34, v51
	v_mul_f32_e32 v187, v34, v52
	v_mul_f32_e32 v188, v34, v53
	v_mul_f32_e32 v189, v34, v54
	v_mul_f32_e32 v190, v34, v55
	v_mul_f32_e32 v191, v34, v56
	v_mul_f32_e32 v192, v34, v57
	ds_read_b128 v[34:37], v184 offset:32
	s_waitcnt lgkmcnt(0)
	v_mfma_f32_32x32x16_f16 v[82:97], v[34:37], v[114:117], 0
	ds_read_b128 v[34:37], v184 offset:4640
	ds_read_b128 v[38:41], v184 offset:9248
	s_nop 9
	s_waitcnt lgkmcnt(0)
	v_mfma_f32_32x32x16_f16 v[66:81], v[34:37], v[114:117], 0
	ds_read_b128 v[34:37], v184 offset:13856
	v_mfma_f32_32x32x16_f16 v[50:65], v[38:41], v[114:117], 0
	s_nop 2
	s_waitcnt lgkmcnt(0)
	v_mfma_f32_32x32x16_f16 v[34:49], v[34:37], v[114:117], 0
	s_nop 1
	s_nop 1
	s_nop 0
	v_exp_f32_e32 v66, v66
	v_exp_f32_e32 v67, v67
	v_exp_f32_e32 v68, v68
	v_exp_f32_e32 v69, v69
	v_cvt_pkrtz_f16_f32 v66, v66, v67
	v_cvt_pkrtz_f16_f32 v67, v68, v69
	v_exp_f32_e32 v68, v70
	v_exp_f32_e32 v69, v71
	v_exp_f32_e32 v70, v72
	v_exp_f32_e32 v71, v73
	v_cvt_pkrtz_f16_f32 v68, v68, v69
	v_cvt_pkrtz_f16_f32 v69, v70, v71
	v_exp_f32_e32 v70, v74
	v_exp_f32_e32 v71, v75
	v_exp_f32_e32 v72, v76
	v_exp_f32_e32 v73, v77
	v_cvt_pkrtz_f16_f32 v70, v70, v71
	v_cvt_pkrtz_f16_f32 v71, v72, v73
	v_exp_f32_e32 v50, v50
	v_exp_f32_e32 v51, v51
	v_exp_f32_e32 v72, v78
	v_exp_f32_e32 v73, v79
	v_exp_f32_e32 v74, v80
	v_exp_f32_e32 v75, v81
	v_exp_f32_e32 v52, v52
	v_exp_f32_e32 v53, v53
	v_cvt_pkrtz_f16_f32 v50, v50, v51
	v_cvt_pkrtz_f16_f32 v72, v72, v73
	v_cvt_pkrtz_f16_f32 v73, v74, v75
	v_and_b32_e32 v74, v143, v50
	v_cvt_pkrtz_f16_f32 v50, v52, v53
	v_and_b32_e32 v75, v144, v50
	v_exp_f32_e32 v50, v54
	v_exp_f32_e32 v51, v55
	v_exp_f32_e32 v52, v56
	v_exp_f32_e32 v53, v57
	v_cvt_pkrtz_f16_f32 v50, v50, v51
	v_and_b32_e32 v76, v145, v50
	v_cvt_pkrtz_f16_f32 v50, v52, v53
	v_and_b32_e32 v77, v146, v50
	v_exp_f32_e32 v50, v58
	v_exp_f32_e32 v51, v59
	v_exp_f32_e32 v52, v60
	v_exp_f32_e32 v53, v61
	v_exp_f32_e32 v82, v82
	v_exp_f32_e32 v83, v83
	v_exp_f32_e32 v84, v84
	v_exp_f32_e32 v85, v85
	v_cvt_pkrtz_f16_f32 v50, v50, v51
	v_and_b32_e32 v78, v147, v50
	v_cvt_pkrtz_f16_f32 v50, v52, v53
	v_cvt_pkrtz_f16_f32 v82, v82, v83
	v_cvt_pkrtz_f16_f32 v83, v84, v85
	v_exp_f32_e32 v84, v86
	v_exp_f32_e32 v85, v87
	v_and_b32_e32 v79, v148, v50
	v_exp_f32_e32 v86, v88
	v_exp_f32_e32 v87, v89
	v_exp_f32_e32 v50, v62
	v_exp_f32_e32 v51, v63
	v_exp_f32_e32 v52, v64
	v_exp_f32_e32 v53, v65
	v_cvt_pkrtz_f16_f32 v84, v84, v85
	v_cvt_pkrtz_f16_f32 v85, v86, v87
	v_cvt_pkrtz_f16_f32 v50, v50, v51
	v_exp_f32_e32 v86, v90
	v_exp_f32_e32 v87, v91
	v_exp_f32_e32 v88, v92
	v_exp_f32_e32 v89, v93
	v_and_b32_e32 v80, v149, v50
	v_cvt_pkrtz_f16_f32 v50, v52, v53
	v_and_b32_e32 v81, v150, v50
	ds_read_b128 v[50:53], v183
	v_cvt_pkrtz_f16_f32 v86, v86, v87
	v_cvt_pkrtz_f16_f32 v87, v88, v89
	v_exp_f32_e32 v88, v94
	v_exp_f32_e32 v89, v95
	v_exp_f32_e32 v90, v96
	v_exp_f32_e32 v91, v97
	v_exp_f32_e32 v34, v34
	v_exp_f32_e32 v35, v35
	v_exp_f32_e32 v36, v36
	v_exp_f32_e32 v37, v37
	v_and_b32_e32 v82, v127, v82
	v_and_b32_e32 v83, v128, v83
	v_and_b32_e32 v84, v129, v84
	v_and_b32_e32 v85, v130, v85
	v_cvt_pkrtz_f16_f32 v88, v88, v89
	v_cvt_pkrtz_f16_f32 v89, v90, v91
	ds_read_b128 v[90:93], v183 offset:32
	s_waitcnt lgkmcnt(0)
	v_mfma_f32_32x32x16_f16 v[50:65], v[50:53], v[82:85], 0
	v_cvt_pkrtz_f16_f32 v34, v34, v35
	v_cvt_pkrtz_f16_f32 v35, v36, v37
	v_exp_f32_e32 v36, v38
	v_exp_f32_e32 v37, v39
	v_exp_f32_e32 v38, v40
	v_exp_f32_e32 v39, v41
	v_and_b32_e32 v86, v131, v86
	v_and_b32_e32 v87, v132, v87
	v_and_b32_e32 v88, v133, v88
	v_and_b32_e32 v89, v134, v89
	v_cvt_pkrtz_f16_f32 v36, v36, v37
	v_cvt_pkrtz_f16_f32 v37, v38, v39
	ds_read_b128 v[38:41], v183 offset:64
	v_mfma_f32_32x32x16_f16 v[50:65], v[90:93], v[86:89], v[50:65]
	v_mov_b32_e32 v115, 0
	v_dot2c_f32_f16_e32 v115, 0x3c003c00, v82
	v_dot2c_f32_f16_e32 v115, 0x3c003c00, v83
	v_dot2c_f32_f16_e32 v115, 0x3c003c00, v84
	v_dot2c_f32_f16_e32 v115, 0x3c003c00, v85
	v_and_b32_e32 v66, v135, v66
	v_and_b32_e32 v67, v136, v67
	v_and_b32_e32 v68, v137, v68
	v_and_b32_e32 v69, v138, v69
	ds_read_b128 v[82:85], v183 offset:96
	s_waitcnt lgkmcnt(0)
	v_mfma_f32_32x32x16_f16 v[50:65], v[38:41], v[66:69], v[50:65]
	v_exp_f32_e32 v42, v42
	v_exp_f32_e32 v43, v43
	v_and_b32_e32 v70, v139, v70
	v_and_b32_e32 v71, v140, v71
	v_and_b32_e32 v72, v141, v72
	v_and_b32_e32 v73, v142, v73
	v_cvt_pkrtz_f16_f32 v38, v42, v43
	v_exp_f32_e32 v39, v44
	v_exp_f32_e32 v44, v45
	ds_read_b128 v[40:43], v183 offset:128
	v_dot2c_f32_f16_e32 v115, 0x3c003c00, v86
	v_mfma_f32_32x32x16_f16 v[50:65], v[82:85], v[70:73], v[50:65]
	v_dot2c_f32_f16_e32 v115, 0x3c003c00, v87
	v_dot2c_f32_f16_e32 v115, 0x3c003c00, v88
	v_dot2c_f32_f16_e32 v115, 0x3c003c00, v89
	v_dot2c_f32_f16_e32 v115, 0x3c003c00, v66
	v_dot2c_f32_f16_e32 v115, 0x3c003c00, v67
	v_dot2c_f32_f16_e32 v115, 0x3c003c00, v68
	v_dot2c_f32_f16_e32 v115, 0x3c003c00, v69
	ds_read_b128 v[66:69], v183 offset:160
	s_waitcnt lgkmcnt(0)
	v_mfma_f32_32x32x16_f16 v[50:65], v[40:43], v[74:77], v[50:65]
	v_dot2c_f32_f16_e32 v115, 0x3c003c00, v70
	v_dot2c_f32_f16_e32 v115, 0x3c003c00, v71
	v_dot2c_f32_f16_e32 v115, 0x3c003c00, v72
	v_cvt_pkrtz_f16_f32 v39, v39, v44
	v_dot2c_f32_f16_e32 v115, 0x3c003c00, v73
	v_exp_f32_e32 v46, v46
	v_exp_f32_e32 v40, v47
	v_exp_f32_e32 v47, v49
	ds_read_b128 v[42:45], v183 offset:192
	v_dot2c_f32_f16_e32 v115, 0x3c003c00, v74
	v_mfma_f32_32x32x16_f16 v[50:65], v[66:69], v[78:81], v[50:65]
	v_dot2c_f32_f16_e32 v115, 0x3c003c00, v75
	v_dot2c_f32_f16_e32 v115, 0x3c003c00, v76
	v_dot2c_f32_f16_e32 v115, 0x3c003c00, v77
	v_exp_f32_e32 v41, v48
	v_dot2c_f32_f16_e32 v115, 0x3c003c00, v78
	v_dot2c_f32_f16_e32 v115, 0x3c003c00, v79
	v_dot2c_f32_f16_e32 v115, 0x3c003c00, v80
	v_dot2c_f32_f16_e32 v115, 0x3c003c00, v81
	v_and_b32_e32 v34, v151, v34
	v_and_b32_e32 v35, v152, v35
	v_and_b32_e32 v36, v153, v36
	v_and_b32_e32 v37, v154, v37
	v_cvt_pkrtz_f16_f32 v40, v46, v40
	v_cvt_pkrtz_f16_f32 v41, v41, v47
	ds_read_b128 v[46:49], v183 offset:224
	v_dot2c_f32_f16_e32 v115, 0x3c003c00, v34
	s_waitcnt lgkmcnt(0)
	v_mfma_f32_32x32x16_f16 v[50:65], v[42:45], v[34:37], v[50:65]
	v_dot2c_f32_f16_e32 v115, 0x3c003c00, v35
	v_dot2c_f32_f16_e32 v115, 0x3c003c00, v36
	v_dot2c_f32_f16_e32 v115, 0x3c003c00, v37
	v_and_b32_e32 v38, v155, v38
	v_dot2c_f32_f16_e32 v115, 0x3c003c00, v38
	v_and_b32_e32 v39, v156, v39
	v_dot2c_f32_f16_e32 v115, 0x3c003c00, v39
	v_and_b32_e32 v40, v157, v40
	v_dot2c_f32_f16_e32 v115, 0x3c003c00, v40
	v_and_b32_e32 v41, v158, v41
	v_dot2c_f32_f16_e32 v115, 0x3c003c00, v41
	s_nop 0
	v_mfma_f32_32x32x16_f16 v[50:65], v[46:49], v[38:41], v[50:65]
	s_nop 0
	v_mov_b32_e32 v34, v115
	v_mov_b32_e32 v35, v115
	s_nop 1
	v_permlane32_swap_b32_e32 v34, v35
	v_cndmask_b32_e64 v34, v34, v35, s[2:3]
	v_add_f32_e32 v34, v115, v34
	v_rcp_f32_e32 v34, v34
	s_nop 2
	v_mul_f32_e32 v52, v34, v58
	v_mul_f32_e32 v53, v34, v59
	v_mul_f32_e32 v54, v34, v60
	v_mul_f32_e32 v55, v34, v61
	v_mul_f32_e32 v56, v34, v62
	v_mul_f32_e32 v57, v34, v63
	v_mul_f32_e32 v58, v34, v64
	v_mul_f32_e32 v59, v34, v65
	v_cvt_pkrtz_f16_f32 v34, v185, v186
	v_cvt_pkrtz_f16_f32 v35, v187, v188
	v_cvt_pkrtz_f16_f32 v36, v189, v190
	v_cvt_pkrtz_f16_f32 v37, v191, v192
	s_and_b64 vcc, exec, s[20:21]
	s_mov_b64 s[20:21], 0
	s_mov_b32 s18, 1
	v_mov_b32_e32 v114, v179
	v_mov_b32_e32 v115, v180
	v_mov_b32_e32 v116, v181
	v_mov_b32_e32 v117, v182
	s_waitcnt vmcnt(0)
	v_mfma_f32_32x32x16_f16 v[2:17], v[240:243], v[34:37], v[2:17]
	v_cvt_pkrtz_f16_f32 v42, v52, v53
	v_cvt_pkrtz_f16_f32 v43, v54, v55
	v_cvt_pkrtz_f16_f32 v44, v56, v57
	v_cvt_pkrtz_f16_f32 v45, v58, v59
	v_mfma_f32_32x32x16_f16 v[18:33], v[236:239], v[34:37], v[18:33]
	v_mov_b32_e32 v34, v175
	v_mov_b32_e32 v35, v176
	v_mov_b32_e32 v36, v177
	v_mov_b32_e32 v37, v178
	v_mfma_f32_32x32x16_f16 v[18:33], v[244:247], v[42:45], v[18:33]
	v_mfma_f32_32x32x16_f16 v[2:17], v[248:251], v[42:45], v[2:17]
	s_cbranch_vccnz .LBB2_83
	v_cvt_f32_f16_sdwa v67, v110 dst_sel:DWORD dst_unused:UNUSED_PAD src0_sel:WORD_1
	v_cvt_f32_f16_e32 v66, v110
	v_cvt_f32_f16_sdwa v69, v111 dst_sel:DWORD dst_unused:UNUSED_PAD src0_sel:WORD_1
	v_cvt_f32_f16_e32 v68, v111
	v_cvt_f32_f16_sdwa v71, v112 dst_sel:DWORD dst_unused:UNUSED_PAD src0_sel:WORD_1
	v_cvt_f32_f16_e32 v70, v112
	v_cvt_f32_f16_sdwa v73, v113 dst_sel:DWORD dst_unused:UNUSED_PAD src0_sel:WORD_1
	v_cvt_f32_f16_e32 v72, v113
	ds_read_b128 v[34:37], v173 offset:7040
	ds_read_b128 v[38:41], v173 offset:7328
	ds_read_b128 v[42:45], v173 offset:7616
	ds_read_b128 v[46:49], v173 offset:7904
	ds_read_b128 v[50:53], v173 offset:8192
	ds_read_b128 v[54:57], v173 offset:8480
	ds_read_b128 v[58:61], v173 offset:8768
	ds_read_b128 v[62:65], v173 offset:9056
	s_waitcnt lgkmcnt(7)
	v_pk_add_f32 v[18:19], v[34:35], v[18:19]
	v_cvt_f32_f16_sdwa v75, v106 dst_sel:DWORD dst_unused:UNUSED_PAD src0_sel:WORD_1
	v_cvt_f32_f16_e32 v74, v106
	v_cvt_f32_f16_sdwa v83, v102 dst_sel:DWORD dst_unused:UNUSED_PAD src0_sel:WORD_1
	v_cvt_f32_f16_e32 v82, v102
	v_pk_add_f32 v[66:67], v[18:19], v[66:67]
	v_pk_add_f32 v[18:19], v[36:37], v[20:21]
	v_cvt_f32_f16_sdwa v77, v107 dst_sel:DWORD dst_unused:UNUSED_PAD src0_sel:WORD_1
	v_cvt_f32_f16_e32 v76, v107
	v_cvt_f32_f16_sdwa v85, v103 dst_sel:DWORD dst_unused:UNUSED_PAD src0_sel:WORD_1
	v_cvt_f32_f16_e32 v84, v103
	v_pk_add_f32 v[68:69], v[18:19], v[68:69]
	s_waitcnt lgkmcnt(6)
	v_pk_add_f32 v[18:19], v[22:23], v[38:39]
	v_cvt_f32_f16_sdwa v79, v108 dst_sel:DWORD dst_unused:UNUSED_PAD src0_sel:WORD_1
	v_cvt_f32_f16_e32 v78, v108
	v_cvt_f32_f16_sdwa v87, v104 dst_sel:DWORD dst_unused:UNUSED_PAD src0_sel:WORD_1
	v_cvt_f32_f16_e32 v86, v104
	v_pk_add_f32 v[70:71], v[18:19], v[70:71]
	v_pk_add_f32 v[18:19], v[24:25], v[40:41]
	v_cvt_f32_f16_sdwa v89, v105 dst_sel:DWORD dst_unused:UNUSED_PAD src0_sel:WORD_1
	v_cvt_f32_f16_e32 v88, v105
	v_pk_add_f32 v[72:73], v[18:19], v[72:73]
	s_waitcnt lgkmcnt(5)
	v_pk_add_f32 v[18:19], v[26:27], v[42:43]
	s_waitcnt lgkmcnt(3)
	v_pk_add_f32 v[2:3], v[50:51], v[2:3]
	v_cvt_f32_f16_sdwa v91, v98 dst_sel:DWORD dst_unused:UNUSED_PAD src0_sel:WORD_1
	v_cvt_f32_f16_e32 v90, v98
	v_pk_add_f32 v[74:75], v[18:19], v[74:75]
	v_pk_add_f32 v[18:19], v[28:29], v[44:45]
	v_pk_add_f32 v[44:45], v[2:3], v[82:83]
	v_pk_add_f32 v[2:3], v[52:53], v[4:5]
	v_cvt_f32_f16_sdwa v93, v99 dst_sel:DWORD dst_unused:UNUSED_PAD src0_sel:WORD_1
	v_cvt_f32_f16_e32 v92, v99
	v_pk_add_f32 v[76:77], v[18:19], v[76:77]
	v_pk_add_f32 v[18:19], v[30:31], v[46:47]
	v_pk_add_f32 v[46:47], v[2:3], v[84:85]
	s_waitcnt lgkmcnt(2)
	v_pk_add_f32 v[2:3], v[6:7], v[54:55]
	v_cvt_f32_f16_sdwa v95, v100 dst_sel:DWORD dst_unused:UNUSED_PAD src0_sel:WORD_1
	v_cvt_f32_f16_e32 v94, v100
	v_pk_add_f32 v[78:79], v[18:19], v[78:79]
	v_pk_add_f32 v[18:19], v[32:33], v[48:49]
	v_pk_add_f32 v[48:49], v[2:3], v[86:87]
	v_pk_add_f32 v[2:3], v[8:9], v[56:57]
	v_cvt_f32_f16_sdwa v97, v101 dst_sel:DWORD dst_unused:UNUSED_PAD src0_sel:WORD_1
	v_cvt_f32_f16_e32 v96, v101
	v_pk_add_f32 v[50:51], v[2:3], v[88:89]
	s_waitcnt lgkmcnt(1)
	v_pk_add_f32 v[2:3], v[10:11], v[58:59]
	v_cvt_f32_f16_sdwa v81, v109 dst_sel:DWORD dst_unused:UNUSED_PAD src0_sel:WORD_1
	v_pk_add_f32 v[52:53], v[2:3], v[90:91]
	v_pk_add_f32 v[2:3], v[12:13], v[60:61]
	v_cvt_f32_f16_e32 v80, v109
	v_pk_add_f32 v[54:55], v[2:3], v[92:93]
	s_waitcnt lgkmcnt(0)
	v_pk_add_f32 v[2:3], v[14:15], v[62:63]
	s_add_i32 s15, 0, 0x16000
	v_pk_add_f32 v[56:57], v[2:3], v[94:95]
	v_pk_add_f32 v[2:3], v[16:17], v[64:65]
	v_pk_add_f32 v[80:81], v[18:19], v[80:81]
	v_pk_add_f32 v[58:59], v[2:3], v[96:97]
	v_add_f32_e32 v3, 0, v66
	v_add_f32_e32 v3, v67, v3
	v_add_f32_e32 v3, v68, v3
	v_add_f32_e32 v3, v69, v3
	v_add_f32_e32 v3, v70, v3
	v_add_f32_e32 v3, v71, v3
	v_add_f32_e32 v3, v72, v3
	v_add_f32_e32 v3, v73, v3
	v_add_f32_e32 v3, v74, v3
	v_add_f32_e32 v3, v75, v3
	v_add_f32_e32 v3, v76, v3
	v_add_f32_e32 v3, v77, v3
	v_add_f32_e32 v3, v78, v3
	v_add_f32_e32 v3, v79, v3
	v_add_f32_e32 v3, v80, v3
	v_add_f32_e32 v3, v81, v3
	v_add_f32_e32 v3, v44, v3
	v_add_f32_e32 v3, v45, v3
	v_add_f32_e32 v3, v46, v3
	v_add_f32_e32 v3, v47, v3
	v_add_f32_e32 v3, v48, v3
	v_add_f32_e32 v3, v49, v3
	v_add_f32_e32 v3, v50, v3
	v_add_f32_e32 v3, v51, v3
	v_add_f32_e32 v3, v52, v3
	v_add_f32_e32 v3, v53, v3
	v_add_f32_e32 v3, v54, v3
	v_add_f32_e32 v3, v55, v3
	v_add_f32_e32 v3, v56, v3
	v_add_f32_e32 v3, v57, v3
	v_add_f32_e32 v3, v58, v3
	v_add_f32_e32 v3, v59, v3
	v_mov_b32_e32 v4, v3
	v_mov_b32_e32 v5, v3
	s_nop 1
	v_permlane32_swap_b32_e32 v4, v5
	v_cndmask_b32_e64 v4, v4, v5, s[2:3]
	v_add_f32_e32 v3, v3, v4
	v_mul_f32_e32 v60, 0x3c800000, v3
	v_or_b32_e32 v3, 0x100, v126
	v_lshrrev_b32_e32 v3, 2, v3
	s_movk_i32 s18, 0x90
	v_mov_b32_e32 v4, s15
	v_pk_add_f32 v[66:67], v[66:67], v[60:61] op_sel_hi:[1,0] neg_lo:[0,1] neg_hi:[0,1]
	v_mad_u32_u24 v3, v3, s18, v4
	v_pk_mul_f32 v[114:115], v[66:67], v[66:67]
	v_pk_add_f32 v[116:117], v[68:69], v[60:61] op_sel_hi:[1,0] neg_lo:[0,1] neg_hi:[0,1]
	ds_read_b128 v[4:7], v3 offset:128
	ds_read_b128 v[8:11], v173 offset:11648
	ds_read_b128 v[12:15], v173 offset:9632
	ds_read_b128 v[16:19], v173 offset:9920
	ds_read_b128 v[20:23], v173 offset:11936
	ds_read_b128 v[24:27], v173 offset:12224
	ds_read_b128 v[28:31], v173 offset:10208
	ds_read_b128 v[32:35], v173 offset:10496
	ds_read_b128 v[36:39], v173 offset:12512
	ds_read_b128 v[40:43], v173 offset:12800
	v_pk_add_f32 v[64:65], v[44:45], v[60:61] op_sel_hi:[1,0] neg_lo:[0,1] neg_hi:[0,1]
	v_pk_add_f32 v[86:87], v[46:47], v[60:61] op_sel_hi:[1,0] neg_lo:[0,1] neg_hi:[0,1]
	v_pk_add_f32 v[88:89], v[48:49], v[60:61] op_sel_hi:[1,0] neg_lo:[0,1] neg_hi:[0,1]
	v_pk_add_f32 v[90:91], v[50:51], v[60:61] op_sel_hi:[1,0] neg_lo:[0,1] neg_hi:[0,1]
	v_pk_add_f32 v[98:99], v[52:53], v[60:61] op_sel_hi:[1,0] neg_lo:[0,1] neg_hi:[0,1]
	v_pk_add_f32 v[100:101], v[54:55], v[60:61] op_sel_hi:[1,0] neg_lo:[0,1] neg_hi:[0,1]
	v_pk_add_f32 v[102:103], v[56:57], v[60:61] op_sel_hi:[1,0] neg_lo:[0,1] neg_hi:[0,1]
	v_pk_add_f32 v[104:105], v[58:59], v[60:61] op_sel_hi:[1,0] neg_lo:[0,1] neg_hi:[0,1]
	v_pk_add_f32 v[78:79], v[78:79], v[60:61] op_sel_hi:[1,0] neg_lo:[0,1] neg_hi:[0,1]
	v_pk_add_f32 v[80:81], v[80:81], v[60:61] op_sel_hi:[1,0] neg_lo:[0,1] neg_hi:[0,1]
	v_pk_add_f32 v[74:75], v[74:75], v[60:61] op_sel_hi:[1,0] neg_lo:[0,1] neg_hi:[0,1]
	v_pk_add_f32 v[76:77], v[76:77], v[60:61] op_sel_hi:[1,0] neg_lo:[0,1] neg_hi:[0,1]
	v_pk_add_f32 v[70:71], v[70:71], v[60:61] op_sel_hi:[1,0] neg_lo:[0,1] neg_hi:[0,1]
	v_pk_add_f32 v[72:73], v[72:73], v[60:61] op_sel_hi:[1,0] neg_lo:[0,1] neg_hi:[0,1]
	v_pk_mul_f32 v[60:61], v[116:117], v[116:117]
	v_add_f32_e32 v3, v114, v115
	v_add_f32_e32 v3, v60, v3
	v_pk_mul_f32 v[110:111], v[70:71], v[70:71]
	v_add_f32_e32 v3, v61, v3
	v_add_f32_e32 v3, v110, v3
	v_pk_mul_f32 v[112:113], v[72:73], v[72:73]
	v_add_f32_e32 v3, v111, v3
	v_add_f32_e32 v3, v112, v3
	v_pk_mul_f32 v[106:107], v[74:75], v[74:75]
	v_add_f32_e32 v3, v113, v3
	v_add_f32_e32 v3, v106, v3
	v_pk_mul_f32 v[108:109], v[76:77], v[76:77]
	v_add_f32_e32 v3, v107, v3
	v_add_f32_e32 v3, v108, v3
	v_pk_mul_f32 v[94:95], v[78:79], v[78:79]
	v_add_f32_e32 v3, v109, v3
	v_add_f32_e32 v3, v94, v3
	v_pk_mul_f32 v[96:97], v[80:81], v[80:81]
	v_add_f32_e32 v3, v95, v3
	v_add_f32_e32 v3, v96, v3
	v_pk_mul_f32 v[62:63], v[64:65], v[64:65]
	v_add_f32_e32 v3, v97, v3
	v_add_f32_e32 v3, v62, v3
	v_pk_mul_f32 v[82:83], v[86:87], v[86:87]
	v_add_f32_e32 v3, v63, v3
	v_add_f32_e32 v3, v82, v3
	v_pk_mul_f32 v[84:85], v[88:89], v[88:89]
	v_add_f32_e32 v3, v83, v3
	v_add_f32_e32 v3, v84, v3
	v_pk_mul_f32 v[92:93], v[90:91], v[90:91]
	v_add_f32_e32 v3, v85, v3
	v_add_f32_e32 v3, v92, v3
	v_pk_mul_f32 v[52:53], v[98:99], v[98:99]
	v_add_f32_e32 v3, v93, v3
	v_add_f32_e32 v3, v52, v3
	v_pk_mul_f32 v[54:55], v[100:101], v[100:101]
	v_add_f32_e32 v3, v53, v3
	v_add_f32_e32 v3, v54, v3
	v_pk_mul_f32 v[56:57], v[102:103], v[102:103]
	v_add_f32_e32 v3, v55, v3
	v_add_f32_e32 v3, v56, v3
	v_pk_mul_f32 v[58:59], v[104:105], v[104:105]
	v_add_f32_e32 v3, v57, v3
	v_add_f32_e32 v3, v58, v3
	v_add_f32_e32 v3, v59, v3
	v_mov_b32_e32 v52, v3
	v_mov_b32_e32 v53, v3
	s_nop 1
	v_permlane32_swap_b32_e32 v52, v53
	v_cndmask_b32_e64 v52, v52, v53, s[2:3]
	v_add_f32_e32 v3, v3, v52
	v_mov_b32_e32 v52, 0x3727c5ac
	v_fmac_f32_e32 v52, 0x3c800000, v3
	v_rsq_f32_e32 v106, v52
	ds_read_b128 v[44:47], v173 offset:10784
	ds_read_b128 v[48:51], v173 offset:11072
	ds_read_b128 v[52:55], v173 offset:13088
	ds_read_b128 v[56:59], v173 offset:13376
	ds_read_b128 v[60:63], v173 offset:11360
	ds_read_b128 v[82:85], v173 offset:13664
	v_mov_b32_e32 v2, 0
	v_pk_mul_f32 v[66:67], v[66:67], v[106:107] op_sel_hi:[1,0]
	s_mov_b32 s15, 8
	s_waitcnt lgkmcnt(14)
	v_pk_fma_f32 v[68:69], v[4:5], v[66:67], v[8:9]
	v_pk_mul_f32 v[4:5], v[116:117], v[106:107] op_sel_hi:[1,0]
	v_mov_b32_e32 v3, v2
	v_pk_fma_f32 v[66:67], v[6:7], v[4:5], v[10:11]
	v_pk_mul_f32 v[4:5], v[70:71], v[106:107] op_sel_hi:[1,0]
	v_mov_b32_e32 v6, v2
	s_waitcnt lgkmcnt(11)
	v_pk_fma_f32 v[70:71], v[12:13], v[4:5], v[20:21]
	v_pk_mul_f32 v[4:5], v[72:73], v[106:107] op_sel_hi:[1,0]
	v_mov_b32_e32 v7, v2
	v_pk_fma_f32 v[72:73], v[14:15], v[4:5], v[22:23]
	v_pk_mul_f32 v[4:5], v[74:75], v[106:107] op_sel_hi:[1,0]
	v_mov_b32_e32 v8, v2
	s_waitcnt lgkmcnt(10)
	v_pk_fma_f32 v[74:75], v[16:17], v[4:5], v[24:25]
	v_pk_mul_f32 v[4:5], v[76:77], v[106:107] op_sel_hi:[1,0]
	v_mov_b32_e32 v9, v2
	v_pk_fma_f32 v[76:77], v[18:19], v[4:5], v[26:27]
	v_pk_mul_f32 v[4:5], v[78:79], v[106:107] op_sel_hi:[1,0]
	v_mov_b32_e32 v10, v2
	s_waitcnt lgkmcnt(7)
	v_pk_fma_f32 v[78:79], v[28:29], v[4:5], v[36:37]
	v_pk_mul_f32 v[4:5], v[80:81], v[106:107] op_sel_hi:[1,0]
	v_mov_b32_e32 v11, v2
	v_pk_fma_f32 v[80:81], v[30:31], v[4:5], v[38:39]
	v_pk_mul_f32 v[4:5], v[64:65], v[106:107] op_sel_hi:[1,0]
	v_mov_b32_e32 v12, v2
	s_waitcnt lgkmcnt(6)
	v_pk_fma_f32 v[96:97], v[32:33], v[4:5], v[40:41]
	v_pk_mul_f32 v[4:5], v[86:87], v[106:107] op_sel_hi:[1,0]
	v_mov_b32_e32 v13, v2
	v_pk_fma_f32 v[94:95], v[34:35], v[4:5], v[42:43]
	v_pk_mul_f32 v[4:5], v[88:89], v[106:107] op_sel_hi:[1,0]
	v_mov_b32_e32 v14, v2
	s_waitcnt lgkmcnt(3)
	v_pk_fma_f32 v[92:93], v[44:45], v[4:5], v[52:53]
	v_pk_mul_f32 v[4:5], v[90:91], v[106:107] op_sel_hi:[1,0]
	v_cvt_pkrtz_f16_f32 v52, v70, v71
	v_pk_fma_f32 v[90:91], v[46:47], v[4:5], v[54:55]
	v_pk_mul_f32 v[4:5], v[98:99], v[106:107] op_sel_hi:[1,0]
	v_cvt_pkrtz_f16_f32 v53, v72, v73
	s_waitcnt lgkmcnt(2)
	v_pk_fma_f32 v[88:89], v[48:49], v[4:5], v[56:57]
	v_pk_mul_f32 v[4:5], v[100:101], v[106:107] op_sel_hi:[1,0]
	v_cvt_pkrtz_f16_f32 v54, v74, v75
	v_pk_fma_f32 v[86:87], v[50:51], v[4:5], v[58:59]
	v_pk_mul_f32 v[4:5], v[102:103], v[106:107] op_sel_hi:[1,0]
	v_cvt_pkrtz_f16_f32 v50, v68, v69
	s_waitcnt lgkmcnt(0)
	v_pk_fma_f32 v[82:83], v[60:61], v[4:5], v[82:83]
	v_pk_mul_f32 v[4:5], v[104:105], v[106:107] op_sel_hi:[1,0]
	v_cvt_pkrtz_f16_f32 v51, v66, v67
	v_pk_fma_f32 v[84:85], v[62:63], v[4:5], v[84:85]
	v_cvt_pkrtz_f16_f32 v55, v76, v77
	v_cvt_pkrtz_f16_f32 v56, v78, v79
	v_cvt_pkrtz_f16_f32 v57, v80, v81
	v_cvt_pkrtz_f16_f32 v58, v96, v97
	v_cvt_pkrtz_f16_f32 v59, v94, v95
	v_cvt_pkrtz_f16_f32 v60, v92, v93
	v_cvt_pkrtz_f16_f32 v61, v90, v91
	v_cvt_pkrtz_f16_f32 v62, v88, v89
	v_cvt_pkrtz_f16_f32 v63, v86, v87
	v_cvt_pkrtz_f16_f32 v64, v82, v83
	v_cvt_pkrtz_f16_f32 v65, v84, v85
	v_mul_u32_u24_e32 v98, 0x90, v164
	v_or_b32_e32 v99, 0x6000, v170
	v_mov_b32_e32 v4, v2
	v_mov_b32_e32 v5, v2
	v_mov_b32_e32 v15, v2
	v_mov_b32_e32 v16, v2
	v_mov_b32_e32 v17, v2
	v_mov_b32_e32 v18, v2
	v_mov_b32_e32 v19, v2
	v_mov_b32_e32 v20, v2
	v_mov_b32_e32 v21, v2
	v_mov_b32_e32 v22, v2
	v_mov_b32_e32 v23, v2
	v_mov_b32_e32 v24, v2
	v_mov_b32_e32 v25, v2
	v_mov_b32_e32 v26, v2
	v_mov_b32_e32 v27, v2
	v_mov_b32_e32 v28, v2
	v_mov_b32_e32 v29, v2
	v_mov_b32_e32 v30, v2
	v_mov_b32_e32 v31, v2
	v_mov_b32_e32 v32, v2
	v_mov_b32_e32 v33, v2

.LBB2_93:
	ds_read_b128 v[18:21], v125 offset:8192
	ds_read_b128 v[34:37], v125 offset:9216
	v_cvt_pkrtz_f16_f32 v50, v74, v75
	v_cvt_pkrtz_f16_f32 v51, v76, v77
	v_cvt_pkrtz_f16_f32 v52, v82, v83
	v_cvt_pkrtz_f16_f32 v53, v84, v85
	v_cvt_pkrtz_f16_f32 v62, v86, v87
	v_cvt_pkrtz_f16_f32 v63, v88, v89
	v_cvt_pkrtz_f16_f32 v64, v94, v95
	s_waitcnt lgkmcnt(0)
	v_mfma_f32_32x32x16_f16 v[18:33], v[18:21], v[50:53], 0
	v_cvt_pkrtz_f16_f32 v65, v110, v111
	ds_read_b128 v[38:41], v125 offset:10240
	v_cvt_pkrtz_f16_f32 v78, v108, v109
	v_cvt_pkrtz_f16_f32 v79, v106, v107
	v_cvt_pkrtz_f16_f32 v80, v104, v105
	v_cvt_pkrtz_f16_f32 v81, v100, v101
	s_add_i32 s0, 0, 0x1a800
	v_mfma_f32_32x32x16_f16 v[18:33], v[34:37], v[62:65], v[18:33]
	v_lshl_add_u32 v99, v165, 1, s0
	ds_read_b128 v[2:5], v125
	ds_read_b128 v[58:61], v125 offset:1024
	ds_read_b128 v[120:123], v125 offset:2048
	ds_read_b128 v[174:177], v125 offset:3072
	ds_read_b128 v[178:181], v125 offset:4096
	ds_read_b128 v[182:185], v125 offset:5120
	ds_read_b128 v[34:37], v125 offset:11264
	ds_read_b128 v[186:189], v125 offset:6144
	ds_read_b128 v[190:193], v125 offset:7168
	v_cvt_pkrtz_f16_f32 v114, v96, v97
	v_cvt_pkrtz_f16_f32 v115, v92, v93
	s_waitcnt lgkmcnt(0)
	v_mfma_f32_32x32x16_f16 v[18:33], v[38:41], v[78:81], v[18:33]
	ds_read_b128 v[194:197], v99 offset:11648
	ds_read_b128 v[198:201], v99 offset:11936
	ds_read_b128 v[38:41], v125 offset:12288
	v_cvt_pkrtz_f16_f32 v116, v90, v91
	v_cvt_pkrtz_f16_f32 v117, v102, v103
	ds_read_b128 v[202:205], v99 offset:12224
	ds_read_b128 v[206:209], v99 offset:12512
	ds_read_b128 v[210:213], v99 offset:12800
	ds_read_b128 v[54:57], v99 offset:13088
	ds_read_b128 v[70:73], v99 offset:13376
	ds_read_b128 v[66:69], v99 offset:13664
	ds_read_b128 v[214:217], v125 offset:13312
	ds_read_b128 v[218:221], v99 offset:13952
	ds_read_b128 v[222:225], v125 offset:14336
	ds_read_b128 v[226:229], v125 offset:15360
	ds_read_b128 v[230:233], v99 offset:14240
	s_mov_b32 s16, 0xff61b1e6
	s_mov_b32 s17, 0
	v_mfma_f32_32x32x16_f16 v[18:33], v[34:37], v[114:117], v[18:33]
	s_waitcnt lgkmcnt(0)
	v_mfma_f32_32x32x16_f16 v[34:49], v[38:41], v[50:53], 0
	s_nop 9
	v_add_f32_e32 v112, v18, v218
	v_add_f32_e32 v113, v19, v219
	v_add_f32_e32 v159, v20, v220
	v_add_f32_e32 v161, v21, v221
	ds_read_b128 v[18:21], v99 offset:14528
	v_add_f32_e32 v164, v22, v230
	v_add_f32_e32 v165, v23, v231
	v_mfma_f32_32x32x16_f16 v[34:49], v[214:217], v[62:65], v[34:49]
	v_add_f32_e32 v170, v24, v232
	v_add_f32_e32 v173, v25, v233
	ds_read_b128 v[22:25], v99 offset:14816
	s_waitcnt lgkmcnt(0)
	v_add_f32_e32 v26, v26, v18
	v_add_f32_e32 v27, v27, v19
	v_add_f32_e32 v28, v28, v20
	v_add_f32_e32 v29, v29, v21
	v_mfma_f32_32x32x16_f16 v[34:49], v[222:225], v[78:81], v[34:49]
	ds_read_b128 v[18:21], v99 offset:15104
	v_add_f32_e32 v30, v30, v22
	v_add_f32_e32 v31, v31, v23
	v_add_f32_e32 v32, v32, v24
	v_add_f32_e32 v33, v33, v25
	ds_read_b128 v[22:25], v99 offset:15392
	v_mfma_f32_32x32x16_f16 v[34:49], v[226:229], v[114:117], v[34:49]
	v_mfma_f32_32x32x16_f16 v[2:17], v[2:5], v[50:53], 0
	s_waitcnt lgkmcnt(0)
	s_nop 9
	v_add_f32_e32 v34, v34, v18
	v_add_f32_e32 v35, v35, v19
	v_add_f32_e32 v36, v36, v20
	v_add_f32_e32 v37, v37, v21
	ds_read_b128 v[18:21], v99 offset:15680
	v_add_f32_e32 v38, v38, v22
	v_add_f32_e32 v39, v39, v23
	v_add_f32_e32 v40, v40, v24
	v_add_f32_e32 v41, v41, v25
	ds_read_b128 v[22:25], v99 offset:15968
	s_waitcnt lgkmcnt(0)
	v_add_f32_e32 v42, v42, v18
	v_add_f32_e32 v43, v43, v19
	v_add_f32_e32 v44, v44, v20
	v_add_f32_e32 v45, v45, v21
	v_cvt_pkrtz_f16_f32 v18, v112, v113
	v_cvt_pkrtz_f16_f32 v19, v159, v161
	v_cvt_pkrtz_f16_f32 v20, v164, v165
	v_cvt_pkrtz_f16_f32 v21, v170, v173
	ds_write_b128 v166, v[18:21]
	v_cvt_pkrtz_f16_f32 v18, v26, v27
	v_cvt_pkrtz_f16_f32 v19, v28, v29
	v_cvt_pkrtz_f16_f32 v20, v30, v31
	v_cvt_pkrtz_f16_f32 v21, v32, v33
	v_add_f32_e32 v22, v46, v22
	v_add_f32_e32 v23, v47, v23
	v_add_f32_e32 v24, v48, v24
	v_add_f32_e32 v25, v49, v25
	ds_write_b128 v166, v[18:21] offset:32
	v_cvt_pkrtz_f16_f32 v18, v34, v35
	v_cvt_pkrtz_f16_f32 v19, v36, v37
	v_cvt_pkrtz_f16_f32 v20, v38, v39
	v_cvt_pkrtz_f16_f32 v21, v40, v41
	ds_write_b128 v166, v[18:21] offset:64
	v_cvt_pkrtz_f16_f32 v18, v42, v43
	v_cvt_pkrtz_f16_f32 v19, v44, v45
	v_cvt_pkrtz_f16_f32 v20, v22, v23
	v_cvt_pkrtz_f16_f32 v21, v24, v25
	ds_write_b128 v166, v[18:21] offset:96
	ds_read_b128 v[18:21], v125 offset:16384
	ds_read_b128 v[22:25], v125 offset:17408
	s_waitcnt lgkmcnt(0)
	v_mfma_f32_32x32x16_f16 v[30:45], v[50:53], v[18:21], 0
	v_add_u32_e32 v112, v167, v162
	v_add_u32_e32 v159, v171, v172
	v_mfma_f32_32x32x16_f16 v[2:17], v[58:61], v[62:65], v[2:17]
	v_mfma_f32_32x32x16_f16 v[30:45], v[62:65], v[22:25], v[30:45]
	ds_read_b128 v[18:21], v125 offset:18432
	ds_read_b128 v[22:25], v125 offset:19456
	v_mfma_f32_32x32x16_f16 v[2:17], v[120:123], v[78:81], v[2:17]
	s_waitcnt lgkmcnt(0)
	v_mfma_f32_32x32x16_f16 v[30:45], v[78:81], v[18:21], v[30:45]
	v_add3_u32 v18, s0, v168, v160
	ds_read_b32 v46, v18 offset:16256
	v_mfma_f32_32x32x16_f16 v[2:17], v[174:177], v[114:117], v[2:17]
	v_mfma_f32_32x32x16_f16 v[30:45], v[114:117], v[22:25], v[30:45]
	s_nop 10
	v_fmamk_f32 v58, v194, 0x3e38aa3b, v2
	v_fmamk_f32 v59, v195, 0x3e38aa3b, v3
	v_fmamk_f32 v99, v198, 0x3e38aa3b, v6
	v_fmamk_f32 v113, v202, 0x3e38aa3b, v10
	v_fmamk_f32 v120, v203, 0x3e38aa3b, v11
	v_fmamk_f32 v121, v204, 0x3e38aa3b, v12
	v_fmamk_f32 v122, v205, 0x3e38aa3b, v13
	s_waitcnt lgkmcnt(0)
	v_add_f32_e32 v2, v46, v30
	v_add_f32_e32 v3, v46, v31
	v_add_f32_e32 v47, v46, v32
	v_add_f32_e32 v48, v46, v33
	v_add_f32_e32 v49, v46, v34
	v_add_f32_e32 v60, v46, v35
	v_add_f32_e32 v61, v46, v36
	v_add_f32_e32 v37, v46, v37
	v_add_f32_e32 v38, v46, v38
	v_add_f32_e32 v39, v46, v39
	v_add_f32_e32 v40, v46, v40
	v_add_f32_e32 v41, v46, v41
	v_add_f32_e32 v42, v46, v42
	v_add_f32_e32 v43, v46, v43
	v_add_f32_e32 v44, v46, v44
	v_add_f32_e32 v45, v46, v45
	v_cvt_pkrtz_f16_f32 v34, v2, v3
	v_cvt_pkrtz_f16_f32 v35, v47, v48
	v_cvt_pkrtz_f16_f32 v36, v49, v60
	v_cvt_pkrtz_f16_f32 v37, v61, v37
	ds_write_b128 v112, v[34:37]
	v_cvt_pkrtz_f16_f32 v34, v38, v39
	v_cvt_pkrtz_f16_f32 v35, v40, v41
	v_cvt_pkrtz_f16_f32 v36, v42, v43
	v_cvt_pkrtz_f16_f32 v37, v44, v45
	ds_write_b128 v112, v[34:37] offset:32
	ds_read_b128 v[34:37], v125 offset:20480
	v_fmamk_f32 v60, v196, 0x3e38aa3b, v4
	v_fmamk_f32 v61, v197, 0x3e38aa3b, v5
	ds_read_b128 v[2:5], v125 offset:21504
	s_waitcnt lgkmcnt(0)
	v_mfma_f32_32x32x16_f16 v[34:49], v[50:53], v[34:37], 0
	v_fmamk_f32 v14, v206, 0x3e38aa3b, v14
	v_fmamk_f32 v15, v207, 0x3e38aa3b, v15
	v_fmamk_f32 v16, v208, 0x3e38aa3b, v16
	v_fmac_f32_e32 v17, 0x3e38aa3b, v209
	v_mfma_f32_32x32x16_f16 v[34:49], v[62:65], v[2:5], v[34:49]
	ds_read_b128 v[2:5], v125 offset:22528
	v_mfma_f32_32x32x16_f16 v[18:33], v[178:181], v[50:53], 0
	v_fmamk_f32 v50, v199, 0x3e38aa3b, v7
	v_fmamk_f32 v51, v200, 0x3e38aa3b, v8
	v_fmamk_f32 v52, v201, 0x3e38aa3b, v9
	ds_read_b128 v[6:9], v125 offset:23552
	s_waitcnt lgkmcnt(0)
	v_mfma_f32_32x32x16_f16 v[34:49], v[78:81], v[2:5], v[34:49]
	v_add3_u32 v2, s0, v169, v160
	ds_read_b32 v2, v2 offset:16256
	s_lshl_b32 s0, s28, 9
	s_add_i32 s0, s0, 0
	s_add_i32 s14, s0, 0x27800
	v_mfma_f32_32x32x16_f16 v[18:33], v[182:185], v[62:65], v[18:33]
	v_mfma_f32_32x32x16_f16 v[34:49], v[114:117], v[6:9], v[34:49]
	v_mfma_f32_32x32x16_f16 v[18:33], v[186:189], v[78:81], v[18:33]
	s_waitcnt lgkmcnt(0)
	s_nop 9
	v_add_f32_e32 v3, v2, v34
	v_add_f32_e32 v4, v2, v35
	v_add_f32_e32 v5, v2, v36
	v_add_f32_e32 v6, v2, v37
	v_add_f32_e32 v7, v2, v38
	v_add_f32_e32 v8, v2, v39
	v_add_f32_e32 v9, v2, v40
	v_add_f32_e32 v10, v2, v41
	v_add_f32_e32 v11, v2, v42
	v_add_f32_e32 v12, v2, v43
	v_add_f32_e32 v13, v2, v44
	v_add_f32_e32 v34, v2, v45
	v_add_f32_e32 v35, v2, v46
	v_add_f32_e32 v36, v2, v47
	v_add_f32_e32 v37, v2, v48
	v_add_f32_e32 v38, v2, v49
	v_cvt_pkrtz_f16_f32 v2, v3, v4
	v_cvt_pkrtz_f16_f32 v3, v5, v6
	v_cvt_pkrtz_f16_f32 v4, v7, v8
	v_cvt_pkrtz_f16_f32 v5, v9, v10
	ds_write_b128 v112, v[2:5] offset:8704
	v_cvt_pkrtz_f16_f32 v2, v11, v12
	v_cvt_pkrtz_f16_f32 v3, v13, v34
	v_cvt_pkrtz_f16_f32 v4, v35, v36
	v_cvt_pkrtz_f16_f32 v5, v37, v38
	ds_write_b128 v112, v[2:5] offset:8736
	s_nop 0
	s_waitcnt lgkmcnt(0)
	s_barrier
	ds_read_b128 v[2:5], v159
	ds_read_b128 v[10:13], v159 offset:32
	v_mfma_f32_32x32x16_f16 v[18:33], v[190:193], v[114:117], v[18:33]
	v_cvt_pkrtz_f16_f32 v6, v58, v59
	v_cvt_pkrtz_f16_f32 v7, v60, v61
	v_cvt_pkrtz_f16_f32 v8, v99, v50
	v_cvt_pkrtz_f16_f32 v9, v51, v52
	v_cvt_pkrtz_f16_f32 v78, v113, v120
	v_cvt_pkrtz_f16_f32 v79, v121, v122
	v_cvt_pkrtz_f16_f32 v80, v14, v15
	s_nop 4
	v_fmamk_f32 v22, v54, 0x3e38aa3b, v22
	v_fmamk_f32 v23, v55, 0x3e38aa3b, v23
	v_fmamk_f32 v24, v56, 0x3e38aa3b, v24
	v_fmamk_f32 v25, v57, 0x3e38aa3b, v25
	s_waitcnt lgkmcnt(1)
	v_mfma_f32_32x32x16_f16 v[50:65], v[2:5], v[6:9], 0
	v_cvt_pkrtz_f16_f32 v81, v16, v17
	ds_read_b128 v[2:5], v159 offset:64
	v_fmamk_f32 v18, v210, 0x3e38aa3b, v18
	v_fmamk_f32 v19, v211, 0x3e38aa3b, v19
	v_fmamk_f32 v20, v212, 0x3e38aa3b, v20
	v_fmamk_f32 v21, v213, 0x3e38aa3b, v21
	v_fmamk_f32 v26, v70, 0x3e38aa3b, v26
	s_waitcnt lgkmcnt(1)
	v_mfma_f32_32x32x16_f16 v[50:65], v[10:13], v[78:81], v[50:65]
	v_fmamk_f32 v27, v71, 0x3e38aa3b, v27
	v_fmamk_f32 v28, v72, 0x3e38aa3b, v28
	v_fmamk_f32 v14, v73, 0x3e38aa3b, v29
	v_cvt_pkrtz_f16_f32 v70, v18, v19
	v_cvt_pkrtz_f16_f32 v71, v20, v21
	v_cvt_pkrtz_f16_f32 v72, v22, v23
	v_cvt_pkrtz_f16_f32 v73, v24, v25
	ds_read_b128 v[10:13], v159 offset:96
	v_fmamk_f32 v15, v66, 0x3e38aa3b, v30
	s_waitcnt lgkmcnt(1)
	v_mfma_f32_32x32x16_f16 v[50:65], v[2:5], v[70:73], v[50:65]
	v_fmamk_f32 v2, v67, 0x3e38aa3b, v31
	v_fmamk_f32 v3, v68, 0x3e38aa3b, v32
	v_fmac_f32_e32 v33, 0x3e38aa3b, v69
	v_cvt_pkrtz_f16_f32 v66, v26, v27
	v_cvt_pkrtz_f16_f32 v67, v28, v14
	v_cvt_pkrtz_f16_f32 v68, v15, v2
	v_cvt_pkrtz_f16_f32 v69, v3, v33
	v_add_u32_e32 v113, v163, v162
	s_waitcnt lgkmcnt(0)
	v_mfma_f32_32x32x16_f16 v[50:65], v[10:13], v[66:69], v[50:65]
	ds_read_b128 v[2:5], v159 offset:4608
	ds_read_b128 v[10:13], v159 offset:4640
	s_waitcnt lgkmcnt(1)
	v_mfma_f32_32x32x16_f16 v[34:49], v[2:5], v[6:9], 0
	s_waitcnt lgkmcnt(0)
	v_mfma_f32_32x32x16_f16 v[34:49], v[10:13], v[78:81], v[34:49]
	ds_read_b128 v[2:5], v159 offset:4672
	ds_read_b128 v[10:13], v159 offset:4704
	s_waitcnt lgkmcnt(1)
	v_mfma_f32_32x32x16_f16 v[34:49], v[2:5], v[70:73], v[34:49]
	s_waitcnt lgkmcnt(0)
	v_mfma_f32_32x32x16_f16 v[34:49], v[10:13], v[66:69], v[34:49]
	ds_read_b128 v[2:5], v159 offset:9216
	ds_read_b128 v[10:13], v159 offset:9248
	s_waitcnt lgkmcnt(1)
	v_mfma_f32_32x32x16_f16 v[18:33], v[2:5], v[6:9], 0
	s_waitcnt lgkmcnt(0)
	v_mfma_f32_32x32x16_f16 v[18:33], v[10:13], v[78:81], v[18:33]
	ds_read_b128 v[2:5], v159 offset:9280
	ds_read_b128 v[10:13], v159 offset:9312
	s_waitcnt lgkmcnt(1)
	v_mfma_f32_32x32x16_f16 v[18:33], v[2:5], v[70:73], v[18:33]
	ds_read_b128 v[2:5], v159 offset:13824
	ds_read_b128 v[114:117], v159 offset:13856
	ds_read_b128 v[120:123], v159 offset:13888
	ds_read_b128 v[164:167], v159 offset:13920
	s_waitcnt lgkmcnt(4)
	v_mfma_f32_32x32x16_f16 v[18:33], v[10:13], v[66:69], v[18:33]
	s_waitcnt lgkmcnt(3)
	v_mfma_f32_32x32x16_f16 v[2:17], v[2:5], v[6:9], 0
	s_waitcnt lgkmcnt(2)
	v_mfma_f32_32x32x16_f16 v[2:17], v[114:117], v[78:81], v[2:17]
	s_waitcnt lgkmcnt(1)
	v_mfma_f32_32x32x16_f16 v[2:17], v[120:123], v[70:73], v[2:17]
	s_waitcnt lgkmcnt(0)
	v_mfma_f32_32x32x16_f16 v[2:17], v[164:167], v[66:69], v[2:17]
	v_mov_b32_e32 v99, 0
	s_nop 10
	s_nop 1
	v_exp_f32_e32 v34, v34
	v_exp_f32_e32 v35, v35
	v_exp_f32_e32 v36, v36
	v_exp_f32_e32 v37, v37
	v_cvt_pkrtz_f16_f32 v34, v34, v35
	v_cvt_pkrtz_f16_f32 v35, v36, v37
	v_exp_f32_e32 v36, v38
	v_exp_f32_e32 v37, v39
	v_exp_f32_e32 v38, v40
	v_exp_f32_e32 v39, v41
	v_exp_f32_e32 v40, v42
	v_exp_f32_e32 v41, v43
	v_exp_f32_e32 v42, v44
	v_exp_f32_e32 v43, v45
	v_cvt_pkrtz_f16_f32 v36, v36, v37
	v_cvt_pkrtz_f16_f32 v37, v38, v39
	v_cvt_pkrtz_f16_f32 v38, v40, v41
	v_cvt_pkrtz_f16_f32 v39, v42, v43
	v_exp_f32_e32 v40, v46
	v_exp_f32_e32 v41, v47
	v_exp_f32_e32 v42, v48
	v_exp_f32_e32 v43, v49
	v_exp_f32_e32 v18, v18
	v_exp_f32_e32 v19, v19
	v_exp_f32_e32 v20, v20
	v_exp_f32_e32 v21, v21
	v_exp_f32_e32 v50, v50
	v_exp_f32_e32 v51, v51
	v_exp_f32_e32 v52, v52
	v_exp_f32_e32 v53, v53
	v_cvt_pkrtz_f16_f32 v40, v40, v41
	v_cvt_pkrtz_f16_f32 v41, v42, v43
	v_cvt_pkrtz_f16_f32 v42, v18, v19
	v_cvt_pkrtz_f16_f32 v43, v20, v21
	v_exp_f32_e32 v18, v22
	v_exp_f32_e32 v19, v23
	v_exp_f32_e32 v20, v24
	v_exp_f32_e32 v21, v25
	v_cvt_pkrtz_f16_f32 v50, v50, v51
	v_cvt_pkrtz_f16_f32 v51, v52, v53
	v_exp_f32_e32 v52, v54
	v_exp_f32_e32 v53, v55
	v_exp_f32_e32 v54, v56
	v_exp_f32_e32 v55, v57
	v_exp_f32_e32 v56, v58
	v_exp_f32_e32 v57, v59
	v_exp_f32_e32 v58, v60
	v_exp_f32_e32 v59, v61
	v_cvt_pkrtz_f16_f32 v44, v18, v19
	v_cvt_pkrtz_f16_f32 v45, v20, v21
	ds_read_b128 v[18:21], v113
	v_exp_f32_e32 v22, v26
	v_exp_f32_e32 v23, v27
	v_cvt_pkrtz_f16_f32 v52, v52, v53
	v_cvt_pkrtz_f16_f32 v53, v54, v55
	v_cvt_pkrtz_f16_f32 v54, v56, v57
	v_cvt_pkrtz_f16_f32 v55, v58, v59
	v_exp_f32_e32 v56, v62
	v_exp_f32_e32 v57, v63
	v_exp_f32_e32 v58, v64
	v_exp_f32_e32 v59, v65
	v_exp_f32_e32 v24, v28
	v_exp_f32_e32 v25, v29
	v_cvt_pkrtz_f16_f32 v46, v22, v23
	v_exp_f32_e32 v48, v30
	v_exp_f32_e32 v49, v31
	v_cvt_pkrtz_f16_f32 v56, v56, v57
	v_cvt_pkrtz_f16_f32 v57, v58, v59
	v_exp_f32_e32 v62, v32
	ds_read_b128 v[58:61], v113 offset:32
	v_cvt_pkrtz_f16_f32 v47, v24, v25
	v_exp_f32_e32 v63, v33
	s_waitcnt lgkmcnt(1)
	v_mfma_f32_32x32x16_f16 v[18:33], v[18:21], v[50:53], 0
	v_cvt_pkrtz_f16_f32 v48, v48, v49
	v_cvt_pkrtz_f16_f32 v49, v62, v63
	ds_read_b128 v[62:65], v113 offset:64
	v_exp_f32_e32 v67, v2
	v_exp_f32_e32 v68, v3
	s_waitcnt lgkmcnt(1)
	v_mfma_f32_32x32x16_f16 v[18:33], v[58:61], v[54:57], v[18:33]
	v_exp_f32_e32 v59, v4
	v_exp_f32_e32 v60, v5
	v_exp_f32_e32 v61, v6
	ds_read_b128 v[2:5], v113 offset:96
	s_waitcnt lgkmcnt(1)
	v_mfma_f32_32x32x16_f16 v[18:33], v[62:65], v[34:37], v[18:33]
	v_exp_f32_e32 v62, v7
	v_exp_f32_e32 v63, v8
	v_exp_f32_e32 v64, v9
	ds_read_b128 v[6:9], v113 offset:128
	s_waitcnt lgkmcnt(1)
	v_mfma_f32_32x32x16_f16 v[18:33], v[2:5], v[38:41], v[18:33]
	v_exp_f32_e32 v10, v10
	ds_read_b128 v[2:5], v113 offset:160
	v_cvt_pkrtz_f16_f32 v58, v67, v68
	v_cvt_pkrtz_f16_f32 v59, v59, v60
	v_cvt_pkrtz_f16_f32 v60, v61, v62
	v_cvt_pkrtz_f16_f32 v61, v63, v64
	s_waitcnt lgkmcnt(1)
	v_mfma_f32_32x32x16_f16 v[18:33], v[6:9], v[42:45], v[18:33]
	v_exp_f32_e32 v11, v11
	v_exp_f32_e32 v12, v12
	v_exp_f32_e32 v13, v13
	ds_read_b128 v[6:9], v113 offset:192
	s_waitcnt lgkmcnt(1)
	v_mfma_f32_32x32x16_f16 v[18:33], v[2:5], v[46:49], v[18:33]
	v_exp_f32_e32 v14, v14
	v_exp_f32_e32 v15, v15
	v_exp_f32_e32 v16, v16
	ds_read_b128 v[2:5], v113 offset:224
	s_waitcnt lgkmcnt(1)
	v_mfma_f32_32x32x16_f16 v[18:33], v[6:9], v[58:61], v[18:33]
	v_exp_f32_e32 v6, v17
	v_cvt_pkrtz_f16_f32 v62, v10, v11
	v_cvt_pkrtz_f16_f32 v63, v12, v13
	v_cvt_pkrtz_f16_f32 v64, v14, v15
	v_cvt_pkrtz_f16_f32 v65, v16, v6
	ds_read_b128 v[6:9], v113 offset:8704
	ds_read_b128 v[66:69], v113 offset:8736
	s_waitcnt lgkmcnt(2)
	v_mfma_f32_32x32x16_f16 v[18:33], v[2:5], v[62:65], v[18:33]
	v_mov_b32_e32 v70, 0
	v_dot2c_f32_f16_e32 v70, 0x3c003c00, v50
	v_dot2c_f32_f16_e32 v70, 0x3c003c00, v51
	v_dot2c_f32_f16_e32 v70, 0x3c003c00, v52
	v_dot2c_f32_f16_e32 v70, 0x3c003c00, v53
	v_dot2c_f32_f16_e32 v70, 0x3c003c00, v54
	v_dot2c_f32_f16_e32 v70, 0x3c003c00, v55
	s_waitcnt lgkmcnt(1)
	v_mfma_f32_32x32x16_f16 v[2:17], v[6:9], v[50:53], 0
	ds_read_b128 v[50:53], v113 offset:8768
	v_dot2c_f32_f16_e32 v70, 0x3c003c00, v56
	v_dot2c_f32_f16_e32 v70, 0x3c003c00, v57
	v_dot2c_f32_f16_e32 v70, 0x3c003c00, v34
	v_dot2c_f32_f16_e32 v70, 0x3c003c00, v35
	v_dot2c_f32_f16_e32 v70, 0x3c003c00, v36
	v_dot2c_f32_f16_e32 v70, 0x3c003c00, v37
	s_waitcnt lgkmcnt(1)
	v_mfma_f32_32x32x16_f16 v[2:17], v[66:69], v[54:57], v[2:17]
	ds_read_b128 v[54:57], v113 offset:8800
	v_dot2c_f32_f16_e32 v70, 0x3c003c00, v38
	v_dot2c_f32_f16_e32 v70, 0x3c003c00, v39
	v_dot2c_f32_f16_e32 v70, 0x3c003c00, v40
	v_dot2c_f32_f16_e32 v70, 0x3c003c00, v41
	v_dot2c_f32_f16_e32 v70, 0x3c003c00, v42
	v_dot2c_f32_f16_e32 v70, 0x3c003c00, v43
	s_waitcnt lgkmcnt(1)
	v_mfma_f32_32x32x16_f16 v[2:17], v[50:53], v[34:37], v[2:17]
	v_dot2c_f32_f16_e32 v70, 0x3c003c00, v44
	ds_read_b128 v[34:37], v113 offset:8832
	v_dot2c_f32_f16_e32 v70, 0x3c003c00, v45
	v_dot2c_f32_f16_e32 v70, 0x3c003c00, v46
	v_dot2c_f32_f16_e32 v70, 0x3c003c00, v47
	v_dot2c_f32_f16_e32 v70, 0x3c003c00, v48
	v_dot2c_f32_f16_e32 v70, 0x3c003c00, v49
	s_waitcnt lgkmcnt(1)
	v_mfma_f32_32x32x16_f16 v[2:17], v[54:57], v[38:41], v[2:17]
	v_dot2c_f32_f16_e32 v70, 0x3c003c00, v58
	v_dot2c_f32_f16_e32 v70, 0x3c003c00, v59
	v_dot2c_f32_f16_e32 v70, 0x3c003c00, v60
	ds_read_b128 v[38:41], v113 offset:8864
	v_dot2c_f32_f16_e32 v70, 0x3c003c00, v61
	v_dot2c_f32_f16_e32 v70, 0x3c003c00, v62
	v_dot2c_f32_f16_e32 v70, 0x3c003c00, v63
	s_waitcnt lgkmcnt(1)
	v_mfma_f32_32x32x16_f16 v[2:17], v[34:37], v[42:45], v[2:17]
	v_dot2c_f32_f16_e32 v70, 0x3c003c00, v64
	v_dot2c_f32_f16_e32 v70, 0x3c003c00, v65
	s_nop 2
	v_mov_b32_e32 v34, v70
	v_mov_b32_e32 v35, v70
	s_nop 1
	v_permlane32_swap_b32_e32 v34, v35
	v_cndmask_b32_e64 v42, v34, v35, s[2:3]
	ds_read_b128 v[34:37], v113 offset:8896
	s_waitcnt lgkmcnt(1)
	v_mfma_f32_32x32x16_f16 v[2:17], v[38:41], v[46:49], v[2:17]
	v_add_f32_e32 v38, v70, v42
	v_rcp_f32_e32 v42, v38
	ds_read_b128 v[38:41], v113 offset:8928
	v_pk_fma_f32 v[78:79], v[42:43], v[18:19], v[74:75] op_sel_hi:[0,1,1]
	v_pk_fma_f32 v[80:81], v[42:43], v[20:21], v[76:77] op_sel_hi:[0,1,1]
	s_waitcnt lgkmcnt(1)
	v_mfma_f32_32x32x16_f16 v[2:17], v[34:37], v[58:61], v[2:17]
	v_fma_f32 v82, v42, v22, v82
	v_fma_f32 v83, v42, v23, v83
	v_fma_f32 v84, v42, v24, v84
	v_fma_f32 v85, v42, v25, v85
	v_fma_f32 v86, v42, v26, v86
	v_fma_f32 v87, v42, v27, v87
	v_pk_fma_f32 v[88:89], v[42:43], v[28:29], v[88:89] op_sel_hi:[0,1,1]
	v_pk_fma_f32 v[72:73], v[42:43], v[30:31], v[94:95] op_sel_hi:[0,1,1]
	v_pk_fma_f32 v[74:75], v[42:43], v[32:33], v[110:111] op_sel_hi:[0,1,1]
	s_waitcnt lgkmcnt(0)
	v_mfma_f32_32x32x16_f16 v[2:17], v[38:41], v[62:65], v[2:17]
	s_nop 11
	v_pk_fma_f32 v[76:77], v[42:43], v[2:3], v[108:109] op_sel_hi:[0,1,1]
	v_pk_fma_f32 v[68:69], v[42:43], v[4:5], v[106:107] op_sel_hi:[0,1,1]
	v_pk_fma_f32 v[70:71], v[42:43], v[6:7], v[104:105] op_sel_hi:[0,1,1]
	v_pk_fma_f32 v[58:59], v[42:43], v[8:9], v[100:101] op_sel_hi:[0,1,1]
	v_pk_fma_f32 v[66:67], v[42:43], v[10:11], v[96:97] op_sel_hi:[0,1,1]
	v_pk_fma_f32 v[60:61], v[42:43], v[12:13], v[92:93] op_sel_hi:[0,1,1]
	v_pk_fma_f32 v[62:63], v[42:43], v[14:15], v[90:91] op_sel_hi:[0,1,1]
	v_pk_fma_f32 v[64:65], v[42:43], v[16:17], v[102:103] op_sel_hi:[0,1,1]
	v_lshl_add_u64 v[2:3], v[118:119], 1, s[4:5]
	v_lshl_add_u64 v[2:3], v[2:3], 0, v[98:99]
	v_cvt_pk_f16_f32 v5, v80, v81
	v_cvt_pk_f16_f32 v4, v78, v79
	s_waitcnt vmcnt(0)
	s_barrier
	global_store_dwordx2 v[2:3], v[4:5], off
	v_cvt_pk_f16_f32 v5, v84, v85
	v_cvt_pk_f16_f32 v4, v82, v83
	global_store_dwordx2 v[2:3], v[4:5], off offset:16
	v_cvt_pk_f16_f32 v5, v88, v89
	v_cvt_pk_f16_f32 v4, v86, v87
	global_store_dwordx2 v[2:3], v[4:5], off offset:32
	v_cvt_pk_f16_f32 v5, v74, v75
	v_cvt_pk_f16_f32 v4, v72, v73
	global_store_dwordx2 v[2:3], v[4:5], off offset:48
	v_cvt_pk_f16_f32 v5, v68, v69
	v_cvt_pk_f16_f32 v4, v76, v77
	global_store_dwordx2 v[2:3], v[4:5], off offset:64
	v_cvt_pk_f16_f32 v5, v58, v59
	v_cvt_pk_f16_f32 v4, v70, v71
	global_store_dwordx2 v[2:3], v[4:5], off offset:80
	v_cvt_pk_f16_f32 v5, v60, v61
	v_cvt_pk_f16_f32 v4, v66, v67
	global_store_dwordx2 v[2:3], v[4:5], off offset:96
	v_cvt_pk_f16_f32 v5, v64, v65
	v_cvt_pk_f16_f32 v4, v62, v63
	v_cmp_gt_u32_e64 s[0:1], 32, v124
	v_lshl_add_u32 v91, v126, 2, s14
	v_lshl_add_u32 v93, v1, 2, s14
	s_mov_b64 s[4:5], -1
	v_mov_b32_e32 v95, v78
	v_mov_b32_e32 v94, v79
	v_mov_b32_e32 v97, v80
	v_mov_b32_e32 v96, v81
	v_mov_b32_e32 v99, v82
	v_mov_b32_e32 v98, v83
	v_mov_b32_e32 v35, v84
	v_mov_b32_e32 v34, v85
	v_mov_b32_e32 v37, v86
	v_mov_b32_e32 v36, v87
	v_mov_b32_e32 v39, v88
	v_mov_b32_e32 v38, v89
	v_mov_b32_e32 v41, v72
	v_mov_b32_e32 v40, v73
	v_mov_b32_e32 v19, v74
	v_mov_b32_e32 v18, v75
	v_mov_b32_e32 v21, v76
	v_mov_b32_e32 v20, v77
	v_mov_b32_e32 v23, v68
	v_mov_b32_e32 v22, v69
	v_mov_b32_e32 v42, v70
	v_mov_b32_e32 v24, v71
	v_mov_b32_e32 v43, v58
	v_mov_b32_e32 v27, v59
	v_mov_b32_e32 v26, v66
	v_mov_b32_e32 v25, v67
	v_mov_b32_e32 v29, v60
	v_mov_b32_e32 v28, v61
	v_mov_b32_e32 v32, v62
	v_mov_b32_e32 v30, v63
	v_mov_b32_e32 v33, v64
	v_mov_b32_e32 v31, v65
	global_store_dwordx2 v[2:3], v[4:5], off offset:112
	s_branch .LBB2_95
.LBB2_94:
	s_or_b64 exec, exec, s[14:15]
	s_waitcnt lgkmcnt(0)
	s_barrier
	ds_read_b128 v[6:9], v91
	v_cndmask_b32_e64 v3, v4, v5, s[2:3]
	v_add_f32_e32 v10, v2, v3
	ds_read_b128 v[2:5], v91 offset:32
	v_mov_b32_e32 v159, 0
	s_waitcnt lgkmcnt(1)
	v_add_f32_e32 v6, v10, v6
	v_mul_f32_e32 v11, 0x3e4ccccd, v6
	v_max_f32_e32 v11, v6, v11
	v_add_f32_e32 v6, v10, v7
	v_mul_f32_e32 v7, 0x3e4ccccd, v6
	v_max_f32_e32 v12, v6, v7
	v_add_f32_e32 v6, v10, v8
	v_mul_f32_e32 v7, 0x3e4ccccd, v6
	v_max_f32_e32 v13, v6, v7
	v_add_f32_e32 v6, v10, v9
	v_mul_f32_e32 v7, 0x3e4ccccd, v6
	s_waitcnt lgkmcnt(0)
	v_add_f32_e32 v2, v10, v2
	v_max_f32_e32 v14, v6, v7
	v_mul_f32_e32 v6, 0x3e4ccccd, v2
	v_max_f32_e32 v15, v2, v6
	v_add_f32_e32 v2, v10, v3
	v_mul_f32_e32 v3, 0x3e4ccccd, v2
	ds_read_b128 v[6:9], v91 offset:64
	v_max_f32_e32 v16, v2, v3
	v_add_f32_e32 v2, v10, v4
	v_mul_f32_e32 v3, 0x3e4ccccd, v2
	v_max_f32_e32 v17, v2, v3
	v_add_f32_e32 v2, v10, v5
	v_mul_f32_e32 v3, 0x3e4ccccd, v2
	v_max_f32_e32 v20, v2, v3
	ds_read_b128 v[2:5], v91 offset:96
	s_waitcnt lgkmcnt(1)
	v_add_f32_e32 v6, v10, v6
	v_mul_f32_e32 v18, 0x3e4ccccd, v6
	v_max_f32_e32 v22, v6, v18
	v_add_f32_e32 v6, v10, v7
	v_mul_f32_e32 v7, 0x3e4ccccd, v6
	v_max_f32_e32 v23, v6, v7
	v_add_f32_e32 v6, v10, v8
	v_mul_f32_e32 v7, 0x3e4ccccd, v6
	v_max_f32_e32 v24, v6, v7
	v_add_f32_e32 v6, v10, v9
	v_mul_f32_e32 v7, 0x3e4ccccd, v6
	s_waitcnt lgkmcnt(0)
	v_add_f32_e32 v2, v10, v2
	v_max_f32_e32 v25, v6, v7
	v_mul_f32_e32 v6, 0x3e4ccccd, v2
	v_max_f32_e32 v26, v2, v6
	v_add_f32_e32 v2, v10, v3
	v_mul_f32_e32 v3, 0x3e4ccccd, v2
	ds_read_b128 v[6:9], v91 offset:128
	v_max_f32_e32 v27, v2, v3
	v_add_f32_e32 v2, v10, v4
	v_mul_f32_e32 v3, 0x3e4ccccd, v2
	v_max_f32_e32 v28, v2, v3
	v_add_f32_e32 v2, v10, v5
	v_mul_f32_e32 v3, 0x3e4ccccd, v2
	v_max_f32_e32 v29, v2, v3
	ds_read_b128 v[2:5], v91 offset:160
	s_waitcnt lgkmcnt(1)
	v_add_f32_e32 v6, v10, v6
	v_mul_f32_e32 v18, 0x3e4ccccd, v6
	v_max_f32_e32 v30, v6, v18
	v_add_f32_e32 v6, v10, v7
	v_mul_f32_e32 v7, 0x3e4ccccd, v6
	v_max_f32_e32 v31, v6, v7
	v_add_f32_e32 v6, v10, v8
	v_mul_f32_e32 v7, 0x3e4ccccd, v6
	v_max_f32_e32 v32, v6, v7
	v_add_f32_e32 v6, v10, v9
	v_mul_f32_e32 v7, 0x3e4ccccd, v6
	s_waitcnt lgkmcnt(0)
	v_add_f32_e32 v2, v10, v2
	v_max_f32_e32 v33, v6, v7
	v_mul_f32_e32 v6, 0x3e4ccccd, v2
	v_max_f32_e32 v40, v2, v6
	v_add_f32_e32 v2, v10, v3
	v_mul_f32_e32 v3, 0x3e4ccccd, v2
	ds_read_b128 v[6:9], v91 offset:192
	v_max_f32_e32 v41, v2, v3
	v_add_f32_e32 v2, v10, v4
	v_mul_f32_e32 v3, 0x3e4ccccd, v2
	v_max_f32_e32 v42, v2, v3
	v_add_f32_e32 v2, v10, v5
	v_mul_f32_e32 v3, 0x3e4ccccd, v2
	v_max_f32_e32 v43, v2, v3
	ds_read_b128 v[2:5], v91 offset:224
	s_waitcnt lgkmcnt(1)
	v_add_f32_e32 v6, v10, v6
	v_mul_f32_e32 v18, 0x3e4ccccd, v6
	v_max_f32_e32 v44, v6, v18
	v_add_f32_e32 v6, v10, v7
	v_mul_f32_e32 v7, 0x3e4ccccd, v6
	v_max_f32_e32 v45, v6, v7
	v_add_f32_e32 v6, v10, v8
	v_mul_f32_e32 v7, 0x3e4ccccd, v6
	v_max_f32_e32 v46, v6, v7
	v_add_f32_e32 v6, v10, v9
	v_mul_f32_e32 v7, 0x3e4ccccd, v6
	s_waitcnt lgkmcnt(0)
	v_add_f32_e32 v2, v10, v2
	v_max_f32_e32 v47, v6, v7
	v_mul_f32_e32 v6, 0x3e4ccccd, v2
	v_max_f32_e32 v48, v2, v6
	v_add_f32_e32 v2, v10, v3
	v_mul_f32_e32 v3, 0x3e4ccccd, v2
	ds_read_b128 v[6:9], v91 offset:256
	v_max_f32_e32 v49, v2, v3
	v_add_f32_e32 v2, v10, v4
	v_mul_f32_e32 v3, 0x3e4ccccd, v2
	v_max_f32_e32 v50, v2, v3
	v_add_f32_e32 v2, v10, v5
	v_mul_f32_e32 v3, 0x3e4ccccd, v2
	v_max_f32_e32 v51, v2, v3
	ds_read_b128 v[2:5], v91 offset:288
	s_waitcnt lgkmcnt(1)
	v_add_f32_e32 v6, v10, v6
	v_mul_f32_e32 v18, 0x3e4ccccd, v6
	v_max_f32_e32 v52, v6, v18
	v_add_f32_e32 v6, v10, v7
	v_mul_f32_e32 v7, 0x3e4ccccd, v6
	v_max_f32_e32 v53, v6, v7
	v_add_f32_e32 v6, v10, v8
	v_mul_f32_e32 v7, 0x3e4ccccd, v6
	v_max_f32_e32 v54, v6, v7
	v_add_f32_e32 v6, v10, v9
	v_mul_f32_e32 v7, 0x3e4ccccd, v6
	s_waitcnt lgkmcnt(0)
	v_add_f32_e32 v2, v10, v2
	v_max_f32_e32 v55, v6, v7
	v_mul_f32_e32 v6, 0x3e4ccccd, v2
	v_max_f32_e32 v56, v2, v6
	v_add_f32_e32 v2, v10, v3
	v_mul_f32_e32 v3, 0x3e4ccccd, v2
	ds_read_b128 v[6:9], v91 offset:320
	v_max_f32_e32 v57, v2, v3
	v_add_f32_e32 v2, v10, v4
	v_mul_f32_e32 v3, 0x3e4ccccd, v2
	v_max_f32_e32 v92, v2, v3
	v_add_f32_e32 v2, v10, v5
	v_mul_f32_e32 v3, 0x3e4ccccd, v2
	v_max_f32_e32 v94, v2, v3
	ds_read_b128 v[2:5], v91 offset:352
	s_waitcnt lgkmcnt(1)
	v_add_f32_e32 v6, v10, v6
	v_mul_f32_e32 v18, 0x3e4ccccd, v6
	v_max_f32_e32 v95, v6, v18
	v_add_f32_e32 v6, v10, v7
	v_mul_f32_e32 v7, 0x3e4ccccd, v6
	v_max_f32_e32 v96, v6, v7
	v_add_f32_e32 v6, v10, v8
	v_mul_f32_e32 v7, 0x3e4ccccd, v6
	v_max_f32_e32 v97, v6, v7
	v_add_f32_e32 v6, v10, v9
	v_mul_f32_e32 v7, 0x3e4ccccd, v6
	s_waitcnt lgkmcnt(0)
	v_add_f32_e32 v2, v10, v2
	v_max_f32_e32 v98, v6, v7
	v_mul_f32_e32 v6, 0x3e4ccccd, v2
	v_max_f32_e32 v99, v2, v6
	v_add_f32_e32 v2, v10, v3
	v_mul_f32_e32 v3, 0x3e4ccccd, v2
	ds_read_b128 v[6:9], v91 offset:384
	v_max_f32_e32 v100, v2, v3
	v_add_f32_e32 v2, v10, v4
	v_mul_f32_e32 v3, 0x3e4ccccd, v2
	v_max_f32_e32 v101, v2, v3
	v_add_f32_e32 v2, v10, v5
	v_mul_f32_e32 v3, 0x3e4ccccd, v2
	v_max_f32_e32 v102, v2, v3
	ds_read_b128 v[2:5], v91 offset:416
	s_waitcnt lgkmcnt(1)
	v_add_f32_e32 v6, v10, v6
	v_mul_f32_e32 v18, 0x3e4ccccd, v6
	v_max_f32_e32 v103, v6, v18
	v_add_f32_e32 v6, v10, v7
	v_mul_f32_e32 v7, 0x3e4ccccd, v6
	v_max_f32_e32 v104, v6, v7
	v_add_f32_e32 v6, v10, v8
	v_mul_f32_e32 v7, 0x3e4ccccd, v6
	v_max_f32_e32 v105, v6, v7
	v_add_f32_e32 v6, v10, v9
	v_mul_f32_e32 v7, 0x3e4ccccd, v6
	s_waitcnt lgkmcnt(0)
	v_add_f32_e32 v2, v10, v2
	v_max_f32_e32 v106, v6, v7
	v_mul_f32_e32 v6, 0x3e4ccccd, v2
	v_max_f32_e32 v107, v2, v6
	v_add_f32_e32 v2, v10, v3
	v_mul_f32_e32 v3, 0x3e4ccccd, v2
	ds_read_b128 v[6:9], v91 offset:448
	v_max_f32_e32 v108, v2, v3
	v_add_f32_e32 v2, v10, v4
	v_mul_f32_e32 v3, 0x3e4ccccd, v2
	v_max_f32_e32 v109, v2, v3
	v_add_f32_e32 v2, v10, v5
	v_mul_f32_e32 v3, 0x3e4ccccd, v2
	v_max_f32_e32 v110, v2, v3
	ds_read_b128 v[2:5], v91 offset:480
	s_waitcnt lgkmcnt(1)
	v_add_f32_e32 v6, v10, v6
	v_mul_f32_e32 v18, 0x3e4ccccd, v6
	v_max_f32_e32 v111, v6, v18
	v_add_f32_e32 v6, v10, v7
	v_mul_f32_e32 v7, 0x3e4ccccd, v6
	v_max_f32_e32 v114, v6, v7
	v_add_f32_e32 v6, v10, v8
	v_mul_f32_e32 v7, 0x3e4ccccd, v6
	v_max_f32_e32 v115, v6, v7
	v_add_f32_e32 v6, v10, v9
	v_mul_f32_e32 v7, 0x3e4ccccd, v6
	s_waitcnt lgkmcnt(0)
	v_add_f32_e32 v2, v10, v2
	v_max_f32_e32 v116, v6, v7
	v_mul_f32_e32 v6, 0x3e4ccccd, v2
	v_max_f32_e32 v117, v2, v6
	v_add_f32_e32 v2, v10, v3
	v_mul_f32_e32 v3, 0x3e4ccccd, v2
	v_max_f32_e32 v120, v2, v3
	v_add_f32_e32 v2, v10, v4
	v_mul_f32_e32 v3, 0x3e4ccccd, v2
	v_max_f32_e32 v121, v2, v3
	v_add_f32_e32 v2, v10, v5
	v_mul_f32_e32 v3, 0x3e4ccccd, v2
	v_max_f32_e32 v122, v2, v3
	s_nop 1
	v_exp_f32_e32 v2, v11
	v_exp_f32_e32 v3, v12
	v_exp_f32_e32 v4, v14
	v_cvt_pkrtz_f16_f32 v2, v2, v3
	v_exp_f32_e32 v3, v13
	v_and_b32_e32 v18, v127, v2
	v_exp_f32_e32 v5, v20
	v_cvt_pkrtz_f16_f32 v2, v3, v4
	v_and_b32_e32 v19, v128, v2
	v_exp_f32_e32 v2, v15
	v_exp_f32_e32 v3, v16
	v_exp_f32_e32 v4, v17
	v_dot2c_f32_f16_e32 v159, 0x3c003c00, v18
	v_cvt_pkrtz_f16_f32 v2, v2, v3
	v_and_b32_e32 v20, v129, v2
	v_cvt_pkrtz_f16_f32 v2, v4, v5
	v_and_b32_e32 v21, v130, v2
	v_exp_f32_e32 v2, v22
	v_exp_f32_e32 v3, v23
	v_exp_f32_e32 v4, v24
	v_exp_f32_e32 v5, v25
	v_cvt_pkrtz_f16_f32 v2, v2, v3
	v_and_b32_e32 v34, v131, v2
	v_cvt_pkrtz_f16_f32 v2, v4, v5
	v_and_b32_e32 v35, v132, v2
	v_exp_f32_e32 v2, v26
	v_exp_f32_e32 v3, v27
	v_exp_f32_e32 v4, v28
	v_exp_f32_e32 v5, v29
	v_cvt_pkrtz_f16_f32 v2, v2, v3
	v_and_b32_e32 v36, v133, v2
	v_cvt_pkrtz_f16_f32 v2, v4, v5
	v_and_b32_e32 v37, v134, v2
	v_exp_f32_e32 v2, v30
	v_exp_f32_e32 v3, v31
	v_exp_f32_e32 v4, v32
	v_exp_f32_e32 v5, v33
	v_cvt_pkrtz_f16_f32 v2, v2, v3
	v_and_b32_e32 v38, v135, v2
	v_cvt_pkrtz_f16_f32 v2, v4, v5
	v_and_b32_e32 v39, v136, v2
	v_exp_f32_e32 v2, v40
	v_exp_f32_e32 v3, v41
	v_exp_f32_e32 v4, v42
	v_exp_f32_e32 v5, v43
	v_cvt_pkrtz_f16_f32 v2, v2, v3
	v_and_b32_e32 v40, v137, v2
	v_cvt_pkrtz_f16_f32 v2, v4, v5
	v_and_b32_e32 v41, v138, v2
	v_exp_f32_e32 v2, v44
	v_exp_f32_e32 v3, v45
	v_exp_f32_e32 v4, v46
	v_exp_f32_e32 v5, v47
	v_cvt_pkrtz_f16_f32 v2, v2, v3
	v_and_b32_e32 v42, v139, v2
	v_cvt_pkrtz_f16_f32 v2, v4, v5
	v_and_b32_e32 v43, v140, v2
	v_exp_f32_e32 v2, v48
	v_exp_f32_e32 v3, v49
	v_exp_f32_e32 v4, v50
	v_exp_f32_e32 v5, v51
	v_cvt_pkrtz_f16_f32 v2, v2, v3
	v_and_b32_e32 v44, v141, v2
	v_cvt_pkrtz_f16_f32 v2, v4, v5
	v_and_b32_e32 v45, v142, v2
	v_exp_f32_e32 v2, v52
	v_exp_f32_e32 v3, v53
	v_exp_f32_e32 v4, v54
	v_exp_f32_e32 v5, v55
	v_cvt_pkrtz_f16_f32 v2, v2, v3
	v_and_b32_e32 v46, v143, v2
	v_cvt_pkrtz_f16_f32 v2, v4, v5
	v_and_b32_e32 v47, v144, v2
	v_exp_f32_e32 v2, v56
	v_exp_f32_e32 v3, v57
	v_exp_f32_e32 v4, v92
	v_exp_f32_e32 v5, v94
	v_cvt_pkrtz_f16_f32 v2, v2, v3
	v_and_b32_e32 v48, v145, v2
	v_cvt_pkrtz_f16_f32 v2, v4, v5
	v_and_b32_e32 v49, v146, v2
	v_exp_f32_e32 v2, v95
	v_exp_f32_e32 v3, v96
	v_exp_f32_e32 v4, v97
	v_exp_f32_e32 v5, v98
	v_cvt_pkrtz_f16_f32 v2, v2, v3
	v_and_b32_e32 v50, v147, v2
	v_cvt_pkrtz_f16_f32 v2, v4, v5
	v_and_b32_e32 v51, v148, v2
	v_exp_f32_e32 v2, v99
	v_exp_f32_e32 v3, v100
	v_exp_f32_e32 v4, v101
	v_exp_f32_e32 v5, v102
	v_cvt_pkrtz_f16_f32 v2, v2, v3
	v_and_b32_e32 v52, v149, v2
	v_cvt_pkrtz_f16_f32 v2, v4, v5
	v_and_b32_e32 v53, v150, v2
	v_exp_f32_e32 v2, v103
	v_exp_f32_e32 v3, v104
	v_exp_f32_e32 v4, v105
	v_exp_f32_e32 v5, v106
	v_cvt_pkrtz_f16_f32 v2, v2, v3
	v_and_b32_e32 v54, v151, v2
	v_exp_f32_e32 v26, v107
	v_cvt_pkrtz_f16_f32 v2, v4, v5
	v_and_b32_e32 v55, v152, v2
	ds_read_b128 v[2:5], v113
	ds_read_b128 v[22:25], v113 offset:32
	v_exp_f32_e32 v27, v108
	v_exp_f32_e32 v28, v109
	s_waitcnt lgkmcnt(1)
	v_mfma_f32_32x32x16_f16 v[2:17], v[2:5], v[18:21], 0
	v_exp_f32_e32 v29, v110
	v_cvt_pkrtz_f16_f32 v26, v26, v27
	v_and_b32_e32 v56, v153, v26
	v_dot2c_f32_f16_e32 v159, 0x3c003c00, v19
	v_cvt_pkrtz_f16_f32 v30, v28, v29
	ds_read_b128 v[26:29], v113 offset:64
	s_waitcnt lgkmcnt(1)
	v_mfma_f32_32x32x16_f16 v[2:17], v[22:25], v[34:37], v[2:17]
	v_and_b32_e32 v57, v154, v30
	v_exp_f32_e32 v30, v111
	v_exp_f32_e32 v31, v114
	ds_read_b128 v[22:25], v113 offset:96
	v_dot2c_f32_f16_e32 v159, 0x3c003c00, v20
	s_waitcnt lgkmcnt(1)
	v_mfma_f32_32x32x16_f16 v[2:17], v[26:29], v[38:41], v[2:17]
	v_cvt_pkrtz_f16_f32 v26, v30, v31
	v_and_b32_e32 v100, v155, v26
	v_exp_f32_e32 v30, v115
	v_exp_f32_e32 v31, v116
	ds_read_b128 v[26:29], v113 offset:128
	s_waitcnt lgkmcnt(1)
	v_mfma_f32_32x32x16_f16 v[2:17], v[22:25], v[42:45], v[2:17]
	v_dot2c_f32_f16_e32 v159, 0x3c003c00, v21
	v_dot2c_f32_f16_e32 v159, 0x3c003c00, v34
	v_dot2c_f32_f16_e32 v159, 0x3c003c00, v35
	v_cvt_pkrtz_f16_f32 v22, v30, v31
	v_dot2c_f32_f16_e32 v159, 0x3c003c00, v36
	v_and_b32_e32 v101, v156, v22
	v_dot2c_f32_f16_e32 v159, 0x3c003c00, v37
	v_exp_f32_e32 v30, v117
	ds_read_b128 v[22:25], v113 offset:160
	v_dot2c_f32_f16_e32 v159, 0x3c003c00, v38
	s_waitcnt lgkmcnt(1)
	v_mfma_f32_32x32x16_f16 v[2:17], v[26:29], v[46:49], v[2:17]
	v_dot2c_f32_f16_e32 v159, 0x3c003c00, v39
	v_dot2c_f32_f16_e32 v159, 0x3c003c00, v40
	v_dot2c_f32_f16_e32 v159, 0x3c003c00, v41
	v_dot2c_f32_f16_e32 v159, 0x3c003c00, v42
	v_dot2c_f32_f16_e32 v159, 0x3c003c00, v43
	v_exp_f32_e32 v31, v120
	v_dot2c_f32_f16_e32 v159, 0x3c003c00, v44
	v_exp_f32_e32 v32, v121
	v_dot2c_f32_f16_e32 v159, 0x3c003c00, v45
	v_exp_f32_e32 v33, v122
	ds_read_b128 v[26:29], v113 offset:192
	v_dot2c_f32_f16_e32 v159, 0x3c003c00, v46
	s_waitcnt lgkmcnt(1)
	v_mfma_f32_32x32x16_f16 v[2:17], v[22:25], v[50:53], v[2:17]
	v_dot2c_f32_f16_e32 v159, 0x3c003c00, v47
	v_dot2c_f32_f16_e32 v159, 0x3c003c00, v48
	v_dot2c_f32_f16_e32 v159, 0x3c003c00, v49
	v_dot2c_f32_f16_e32 v159, 0x3c003c00, v50
	v_dot2c_f32_f16_e32 v159, 0x3c003c00, v51
	v_cvt_pkrtz_f16_f32 v22, v30, v31
	v_dot2c_f32_f16_e32 v159, 0x3c003c00, v52
	v_and_b32_e32 v102, v157, v22
	v_cvt_pkrtz_f16_f32 v22, v32, v33
	v_dot2c_f32_f16_e32 v159, 0x3c003c00, v53
	v_and_b32_e32 v103, v158, v22
	ds_read_b128 v[22:25], v113 offset:224
	v_dot2c_f32_f16_e32 v159, 0x3c003c00, v54
	s_waitcnt lgkmcnt(1)
	v_mfma_f32_32x32x16_f16 v[2:17], v[26:29], v[54:57], v[2:17]
	v_dot2c_f32_f16_e32 v159, 0x3c003c00, v55
	v_dot2c_f32_f16_e32 v159, 0x3c003c00, v56
	v_dot2c_f32_f16_e32 v159, 0x3c003c00, v57
	v_dot2c_f32_f16_e32 v159, 0x3c003c00, v100
	v_dot2c_f32_f16_e32 v159, 0x3c003c00, v101
	v_dot2c_f32_f16_e32 v159, 0x3c003c00, v102
	v_dot2c_f32_f16_e32 v159, 0x3c003c00, v103
	s_waitcnt lgkmcnt(0)
	v_mfma_f32_32x32x16_f16 v[2:17], v[22:25], v[100:103], v[2:17]
	s_xor_b64 s[14:15], s[4:5], -1
	s_mov_b32 s17, 1
	v_mov_b32_e32 v26, v159
	v_mov_b32_e32 v27, v159
	s_nop 1
	v_permlane32_swap_b32_e32 v26, v27
	v_cndmask_b32_e64 v26, v26, v27, s[2:3]
	v_add_f32_e32 v26, v159, v26
	v_rcp_f32_e32 v92, v26
	s_mov_b64 s[4:5], 0
	s_nop 0
	v_pk_mul_f32 v[2:3], v[92:93], v[2:3] op_sel_hi:[0,1]
	v_mul_f32_e32 v22, 0x3fb8aa3b, v2
	v_mul_f32_e32 v23, 0x3fb8aa3b, v3
	v_exp_f32_e32 v22, v22
	v_exp_f32_e32 v23, v23
	v_pk_mul_f32 v[24:25], v[92:93], v[4:5] op_sel_hi:[0,1]
	v_mul_f32_e32 v4, 0x3fb8aa3b, v24
	v_mul_f32_e32 v5, 0x3fb8aa3b, v25
	v_pk_add_f32 v[22:23], v[22:23], -1.0 op_sel_hi:[1,0]
	v_exp_f32_e32 v4, v4
	v_exp_f32_e32 v5, v5
	v_cmp_lt_f32_e32 vcc, 0, v3
	v_pk_mul_f32 v[104:105], v[92:93], v[6:7] op_sel_hi:[0,1]
	v_pk_mul_f32 v[108:109], v[92:93], v[8:9] op_sel_hi:[0,1]
	v_cndmask_b32_e32 v94, v23, v3, vcc
	v_cmp_lt_f32_e32 vcc, 0, v2
	v_pk_mul_f32 v[10:11], v[92:93], v[10:11] op_sel_hi:[0,1]
	v_pk_mul_f32 v[12:13], v[92:93], v[12:13] op_sel_hi:[0,1]
	v_cndmask_b32_e32 v95, v22, v2, vcc
	v_mul_f32_e32 v2, 0x3fb8aa3b, v104
	v_exp_f32_e32 v6, v2
	v_mul_f32_e32 v2, 0x3fb8aa3b, v105
	v_pk_add_f32 v[22:23], v[4:5], -1.0 op_sel_hi:[1,0]
	v_exp_f32_e32 v7, v2
	ds_read_b128 v[2:5], v113 offset:8704
	v_cmp_lt_f32_e32 vcc, 0, v25
	v_pk_mul_f32 v[14:15], v[92:93], v[14:15] op_sel_hi:[0,1]
	v_pk_add_f32 v[106:107], v[6:7], -1.0 op_sel_hi:[1,0]
	v_mul_f32_e32 v6, 0x3fb8aa3b, v108
	v_cndmask_b32_e32 v96, v23, v25, vcc
	v_cmp_lt_f32_e32 vcc, 0, v24
	v_exp_f32_e32 v110, v6
	ds_read_b128 v[6:9], v113 offset:8736
	v_cndmask_b32_e32 v97, v22, v24, vcc
	s_waitcnt lgkmcnt(1)
	v_mfma_f32_32x32x16_f16 v[18:33], v[2:5], v[18:21], 0
	v_mul_f32_e32 v2, 0x3fb8aa3b, v109
	v_exp_f32_e32 v111, v2
	ds_read_b128 v[2:5], v113 offset:8768
	v_cmp_lt_f32_e32 vcc, 0, v105
	s_nop 1
	v_cndmask_b32_e32 v98, v107, v105, vcc
	s_waitcnt lgkmcnt(1)
	v_mfma_f32_32x32x16_f16 v[18:33], v[6:9], v[34:37], v[18:33]
	v_mul_f32_e32 v6, 0x3fb8aa3b, v10
	v_exp_f32_e32 v36, v6
	v_mul_f32_e32 v6, 0x3fb8aa3b, v11
	v_exp_f32_e32 v37, v6
	ds_read_b128 v[6:9], v113 offset:8800
	v_cmp_lt_f32_e32 vcc, 0, v104
	s_waitcnt lgkmcnt(1)
	v_mfma_f32_32x32x16_f16 v[18:33], v[2:5], v[38:41], v[18:33]
	v_mul_f32_e32 v2, 0x3fb8aa3b, v12
	v_exp_f32_e32 v40, v2
	ds_read_b128 v[2:5], v113 offset:8832
	v_pk_add_f32 v[38:39], v[36:37], -1.0 op_sel_hi:[1,0]
	v_mul_f32_e32 v36, 0x3fb8aa3b, v13
	v_cndmask_b32_e32 v99, v106, v104, vcc
	v_pk_add_f32 v[104:105], v[110:111], -1.0 op_sel_hi:[1,0]
	s_waitcnt lgkmcnt(1)
	v_mfma_f32_32x32x16_f16 v[18:33], v[6:9], v[42:45], v[18:33]
	ds_read_b128 v[6:9], v113 offset:8864
	v_cmp_lt_f32_e32 vcc, 0, v109
	v_exp_f32_e32 v41, v36
	s_nop 0
	v_cndmask_b32_e32 v34, v105, v109, vcc
	v_cmp_lt_f32_e32 vcc, 0, v108
	s_waitcnt lgkmcnt(1)
	v_mfma_f32_32x32x16_f16 v[18:33], v[2:5], v[46:49], v[18:33]
	v_cndmask_b32_e32 v35, v104, v108, vcc
	v_cmp_lt_f32_e32 vcc, 0, v11
	v_mul_f32_e32 v2, 0x3fb8aa3b, v14
	s_nop 0
	v_cndmask_b32_e32 v36, v39, v11, vcc
	v_cmp_lt_f32_e32 vcc, 0, v10
	s_waitcnt lgkmcnt(0)
	v_mfma_f32_32x32x16_f16 v[18:33], v[6:9], v[50:53], v[18:33]
	v_cndmask_b32_e32 v37, v38, v10, vcc
	v_add_f32_e64 v10, v40, -1.0
	v_add_f32_e64 v11, v41, -1.0
	v_exp_f32_e32 v40, v2
	v_mul_f32_e32 v2, 0x3fb8aa3b, v15
	v_exp_f32_e32 v41, v2
	ds_read_b128 v[2:5], v113 offset:8896
	v_cmp_lt_f32_e32 vcc, 0, v13
	s_nop 1
	v_cndmask_b32_e32 v38, v11, v13, vcc
	v_cmp_lt_f32_e32 vcc, 0, v12
	s_nop 1
	v_cndmask_b32_e32 v39, v10, v12, vcc
	v_pk_mul_f32 v[12:13], v[92:93], v[16:17] op_sel_hi:[0,1]
	v_mul_f32_e32 v6, 0x3fb8aa3b, v12
	v_exp_f32_e32 v16, v6
	ds_read_b128 v[6:9], v113 offset:8928
	s_waitcnt lgkmcnt(1)
	v_mfma_f32_32x32x16_f16 v[18:33], v[2:5], v[54:57], v[18:33]
	v_mul_f32_e32 v2, 0x3fb8aa3b, v13
	v_exp_f32_e32 v17, v2
	v_pk_add_f32 v[10:11], v[40:41], -1.0 op_sel_hi:[1,0]
	v_cmp_lt_f32_e32 vcc, 0, v15
	s_waitcnt lgkmcnt(0)
	v_pk_add_f32 v[2:3], v[16:17], -1.0 op_sel_hi:[1,0]
	v_cndmask_b32_e32 v40, v11, v15, vcc
	v_mfma_f32_32x32x16_f16 v[18:33], v[6:9], v[100:103], v[18:33]
	v_cmp_lt_f32_e32 vcc, 0, v14
	s_barrier
	s_nop 0
	v_cndmask_b32_e32 v41, v10, v14, vcc
	v_cmp_lt_f32_e32 vcc, 0, v13
	s_nop 6
	v_pk_mul_f32 v[4:5], v[92:93], v[18:19] op_sel_hi:[0,1]
	v_mul_f32_e32 v6, 0x3fb8aa3b, v4
	v_mul_f32_e32 v7, 0x3fb8aa3b, v5
	v_exp_f32_e32 v6, v6
	v_exp_f32_e32 v7, v7
	v_cndmask_b32_e32 v18, v3, v13, vcc
	v_cmp_lt_f32_e32 vcc, 0, v12
	s_nop 1
	v_cndmask_b32_e32 v19, v2, v12, vcc
	v_pk_add_f32 v[2:3], v[6:7], -1.0 op_sel_hi:[1,0]
	v_pk_mul_f32 v[6:7], v[92:93], v[20:21] op_sel_hi:[0,1]
	v_mul_f32_e32 v8, 0x3fb8aa3b, v6
	v_mul_f32_e32 v9, 0x3fb8aa3b, v7
	v_exp_f32_e32 v8, v8
	v_exp_f32_e32 v9, v9
	v_cmp_lt_f32_e32 vcc, 0, v5
	s_nop 1
	v_cndmask_b32_e32 v20, v3, v5, vcc
	v_cmp_lt_f32_e32 vcc, 0, v4
	s_nop 1
	v_cndmask_b32_e32 v21, v2, v4, vcc
	v_pk_mul_f32 v[4:5], v[92:93], v[22:23] op_sel_hi:[0,1]
	v_pk_add_f32 v[2:3], v[8:9], -1.0 op_sel_hi:[1,0]
	v_mul_f32_e32 v8, 0x3fb8aa3b, v4
	v_mul_f32_e32 v9, 0x3fb8aa3b, v5
	v_exp_f32_e32 v8, v8
	v_exp_f32_e32 v9, v9
	v_cmp_lt_f32_e32 vcc, 0, v7
	s_nop 1
	v_cndmask_b32_e32 v22, v3, v7, vcc
	v_cmp_lt_f32_e32 vcc, 0, v6
	s_nop 1
	v_cndmask_b32_e32 v23, v2, v6, vcc
	v_pk_mul_f32 v[6:7], v[92:93], v[24:25] op_sel_hi:[0,1]
	v_pk_add_f32 v[2:3], v[8:9], -1.0 op_sel_hi:[1,0]
	v_mul_f32_e32 v8, 0x3fb8aa3b, v6
	v_mul_f32_e32 v9, 0x3fb8aa3b, v7
	v_exp_f32_e32 v8, v8
	v_exp_f32_e32 v9, v9
	v_cmp_lt_f32_e32 vcc, 0, v5
	s_nop 1
	v_cndmask_b32_e32 v24, v3, v5, vcc
	v_cmp_lt_f32_e32 vcc, 0, v4
	s_nop 1
	v_cndmask_b32_e32 v42, v2, v4, vcc
	v_pk_mul_f32 v[4:5], v[92:93], v[26:27] op_sel_hi:[0,1]
	v_pk_add_f32 v[2:3], v[8:9], -1.0 op_sel_hi:[1,0]
	v_mul_f32_e32 v8, 0x3fb8aa3b, v4
	v_mul_f32_e32 v9, 0x3fb8aa3b, v5
	v_exp_f32_e32 v8, v8
	v_exp_f32_e32 v9, v9
	v_cmp_lt_f32_e32 vcc, 0, v7
	s_nop 1
	v_cndmask_b32_e32 v27, v3, v7, vcc
	v_cmp_lt_f32_e32 vcc, 0, v6
	s_nop 1
	v_cndmask_b32_e32 v43, v2, v6, vcc
	v_pk_mul_f32 v[6:7], v[92:93], v[28:29] op_sel_hi:[0,1]
	v_pk_add_f32 v[2:3], v[8:9], -1.0 op_sel_hi:[1,0]
	v_mul_f32_e32 v8, 0x3fb8aa3b, v6
	v_mul_f32_e32 v9, 0x3fb8aa3b, v7
	v_exp_f32_e32 v8, v8
	v_exp_f32_e32 v9, v9
	v_cmp_lt_f32_e32 vcc, 0, v5
	s_nop 1
	v_cndmask_b32_e32 v25, v3, v5, vcc
	v_cmp_lt_f32_e32 vcc, 0, v4
	s_nop 1
	v_cndmask_b32_e32 v26, v2, v4, vcc
	v_pk_mul_f32 v[4:5], v[92:93], v[30:31] op_sel_hi:[0,1]
	v_pk_add_f32 v[2:3], v[8:9], -1.0 op_sel_hi:[1,0]
	v_mul_f32_e32 v8, 0x3fb8aa3b, v4
	v_mul_f32_e32 v9, 0x3fb8aa3b, v5
	v_exp_f32_e32 v8, v8
	v_exp_f32_e32 v9, v9
	v_cmp_lt_f32_e32 vcc, 0, v7
	s_nop 1
	v_cndmask_b32_e32 v28, v3, v7, vcc
	v_cmp_lt_f32_e32 vcc, 0, v6
	s_nop 1
	v_cndmask_b32_e32 v29, v2, v6, vcc
	v_pk_mul_f32 v[6:7], v[92:93], v[32:33] op_sel_hi:[0,1]
	v_pk_add_f32 v[2:3], v[8:9], -1.0 op_sel_hi:[1,0]
	v_mul_f32_e32 v8, 0x3fb8aa3b, v6
	v_mul_f32_e32 v9, 0x3fb8aa3b, v7
	v_exp_f32_e32 v8, v8
	v_exp_f32_e32 v9, v9
	v_cmp_lt_f32_e32 vcc, 0, v5
	s_nop 1
	v_cndmask_b32_e32 v30, v3, v5, vcc
	v_cmp_lt_f32_e32 vcc, 0, v4
	s_nop 1
	v_cndmask_b32_e32 v32, v2, v4, vcc
	v_pk_add_f32 v[2:3], v[8:9], -1.0 op_sel_hi:[1,0]
	v_cmp_lt_f32_e32 vcc, 0, v7
	s_nop 1
	v_cndmask_b32_e32 v31, v3, v7, vcc
	v_cmp_lt_f32_e32 vcc, 0, v6
	s_nop 1
	v_cndmask_b32_e32 v33, v2, v6, vcc
	s_and_b64 vcc, exec, s[14:15]
	s_cbranch_vccnz .LBB2_97

	.amdhsa_kernel _Z10k2_featurePKfPKDF16_S0_S0_S0_S0_S0_S0_PKyS0_S0_S0_S0_S0_S0_S0_PfS5_S5_S5_S5_
		.amdhsa_group_segment_fixed_size 0
		.amdhsa_private_segment_fixed_size 0
		.amdhsa_kernarg_size 168
		.amdhsa_user_sgpr_count 2
		.amdhsa_user_sgpr_dispatch_ptr 0
		.amdhsa_user_sgpr_queue_ptr 0
		.amdhsa_user_sgpr_kernarg_segment_ptr 1
		.amdhsa_user_sgpr_dispatch_id 0
		.amdhsa_user_sgpr_kernarg_preload_length 0
		.amdhsa_user_sgpr_kernarg_preload_offset 0
		.amdhsa_user_sgpr_private_segment_size 0
		.amdhsa_uses_dynamic_stack 0
		.amdhsa_enable_private_segment 0
		.amdhsa_system_sgpr_workgroup_id_x 1
		.amdhsa_system_sgpr_workgroup_id_y 0
		.amdhsa_system_sgpr_workgroup_id_z 0
		.amdhsa_system_sgpr_workgroup_info 0
		.amdhsa_system_vgpr_workitem_id 0
		.amdhsa_next_free_vgpr 256
		.amdhsa_next_free_sgpr 32
		.amdhsa_accum_offset 256
		.amdhsa_reserve_vcc 1
		.amdhsa_float_round_mode_32 0
		.amdhsa_float_round_mode_16_64 0
		.amdhsa_float_denorm_mode_32 3
		.amdhsa_float_denorm_mode_16_64 3
		.amdhsa_dx10_clamp 1
		.amdhsa_ieee_mode 1
		.amdhsa_fp16_overflow 0
		.amdhsa_tg_split 0
		.amdhsa_exception_fp_ieee_invalid_op 0
		.amdhsa_exception_fp_denorm_src 0
		.amdhsa_exception_fp_ieee_div_zero 0
		.amdhsa_exception_fp_ieee_overflow 0
		.amdhsa_exception_fp_ieee_underflow 0
		.amdhsa_exception_fp_ieee_inexact 0
		.amdhsa_exception_int_div_zero 0
	.end_amdhsa_kernel

amdhsa.kernels:
  - .agpr_count:     0
    .args:
      - .offset:         0
        .size:           272
        .value_kind:     by_value
    .group_segment_fixed_size: 27780
    .kernarg_segment_align: 8
    .kernarg_segment_size: 272
    .language:       OpenCL C
    .language_version:
      - 2
      - 0
    .max_flat_workgroup_size: 1024
    .name:           _Z6k_prep5PrepP
    .private_segment_fixed_size: 0
    .sgpr_count:     106
    .sgpr_spill_count: 0
    .symbol:         _Z6k_prep5PrepP.kd
    .uniform_work_group_size: 1
    .uses_dynamic_stack: false
    .vgpr_count:     67
    .vgpr_spill_count: 0
    .wavefront_size: 64
  - .agpr_count:     0
    .args:
      - .actual_access:  read_only
        .address_space:  global
        .offset:         0
        .size:           8
        .value_kind:     global_buffer
      - .actual_access:  read_only
        .address_space:  global
        .offset:         8
        .size:           8
        .value_kind:     global_buffer
      - .actual_access:  read_only
        .address_space:  global
        .offset:         16
        .size:           8
        .value_kind:     global_buffer
      - .address_space:  global
        .offset:         24
        .size:           8
        .value_kind:     global_buffer
      - .actual_access:  read_only
        .address_space:  global
        .offset:         32
        .size:           8
        .value_kind:     global_buffer
      - .actual_access:  read_only
        .address_space:  global
        .offset:         40
        .size:           8
        .value_kind:     global_buffer
      - .actual_access:  read_only
        .address_space:  global
        .offset:         48
        .size:           8
        .value_kind:     global_buffer
      - .actual_access:  read_only
        .address_space:  global
        .offset:         56
        .size:           8
        .value_kind:     global_buffer
      - .actual_access:  write_only
        .address_space:  global
        .offset:         64
        .size:           8
        .value_kind:     global_buffer
    .group_segment_fixed_size: 0
    .kernarg_segment_align: 8
    .kernarg_segment_size: 72
    .language:       OpenCL C
    .language_version:
      - 2
      - 0
    .max_flat_workgroup_size: 384
    .name:           _Z11k1_temporalPKfS0_S0_PKDF16_S0_S0_S0_S0_Pf
    .private_segment_fixed_size: 0
    .sgpr_count:     34
    .sgpr_spill_count: 0
    .symbol:         _Z11k1_temporalPKfS0_S0_PKDF16_S0_S0_S0_S0_Pf.kd
    .uniform_work_group_size: 1
    .uses_dynamic_stack: false
    .vgpr_count:     247
    .vgpr_spill_count: 0
    .wavefront_size: 64
  - .agpr_count:     0
    .args:
      - .address_space:  global
        .offset:         0
        .size:           8
        .value_kind:     global_buffer
      - .address_space:  global
        .offset:         8
        .size:           8
        .value_kind:     global_buffer
      - .actual_access:  read_only
        .address_space:  global
        .offset:         16
        .size:           8
        .value_kind:     global_buffer
      - .actual_access:  read_only
        .address_space:  global
        .offset:         24
        .size:           8
        .value_kind:     global_buffer
      - .actual_access:  read_only
        .address_space:  global
        .offset:         32
        .size:           8
        .value_kind:     global_buffer
      - .actual_access:  read_only
        .address_space:  global
        .offset:         40
        .size:           8
        .value_kind:     global_buffer
      - .actual_access:  read_only
        .address_space:  global
        .offset:         48
        .size:           8
        .value_kind:     global_buffer
      - .actual_access:  read_only
        .address_space:  global
        .offset:         56
        .size:           8
        .value_kind:     global_buffer
      - .actual_access:  read_only
        .address_space:  global
        .offset:         64
        .size:           8
        .value_kind:     global_buffer
      - .actual_access:  read_only
        .address_space:  global
        .offset:         72
        .size:           8
        .value_kind:     global_buffer
      - .actual_access:  read_only
        .address_space:  global
        .offset:         80
        .size:           8
        .value_kind:     global_buffer
      - .actual_access:  read_only
        .address_space:  global
        .offset:         88
        .size:           8
        .value_kind:     global_buffer
      - .actual_access:  read_only
        .address_space:  global
        .offset:         96
        .size:           8
        .value_kind:     global_buffer
      - .actual_access:  read_only
        .address_space:  global
        .offset:         104
        .size:           8
        .value_kind:     global_buffer
      - .actual_access:  read_only
        .address_space:  global
        .offset:         112
        .size:           8
        .value_kind:     global_buffer
      - .actual_access:  read_only
        .address_space:  global
        .offset:         120
        .size:           8
        .value_kind:     global_buffer
      - .address_space:  global
        .offset:         128
        .size:           8
        .value_kind:     global_buffer
      - .actual_access:  write_only
        .address_space:  global
        .offset:         136
        .size:           8
        .value_kind:     global_buffer
      - .actual_access:  write_only
        .address_space:  global
        .offset:         144
        .size:           8
        .value_kind:     global_buffer
      - .actual_access:  write_only
        .address_space:  global
        .offset:         152
        .size:           8
        .value_kind:     global_buffer
      - .actual_access:  write_only
        .address_space:  global
        .offset:         160
        .size:           8
        .value_kind:     global_buffer
    .group_segment_fixed_size: 0
    .kernarg_segment_align: 8
    .kernarg_segment_size: 168
    .language:       OpenCL C
    .language_version:
      - 2
      - 0
    .max_flat_workgroup_size: 512
    .name:           _Z10k2_featurePKfPKDF16_S0_S0_S0_S0_S0_S0_PKyS0_S0_S0_S0_S0_S0_S0_PfS5_S5_S5_S5_
    .private_segment_fixed_size: 0
    .sgpr_count:     38
    .sgpr_spill_count: 0
    .symbol:         _Z10k2_featurePKfPKDF16_S0_S0_S0_S0_S0_S0_PKyS0_S0_S0_S0_S0_S0_S0_PfS5_S5_S5_S5_.kd
    .uniform_work_group_size: 1
    .uses_dynamic_stack: false
    .vgpr_count:     256
    .vgpr_spill_count: 0
    .wavefront_size: 64
  - .agpr_count:     0
    .args:
      - .actual_access:  read_only
        .address_space:  global
        .offset:         0
        .size:           8
        .value_kind:     global_buffer
      - .actual_access:  read_only
        .address_space:  global
        .offset:         8
        .size:           8
        .value_kind:     global_buffer
      - .actual_access:  read_only
        .address_space:  global
        .offset:         16
        .size:           8
        .value_kind:     global_buffer
      - .actual_access:  read_only
        .address_space:  global
        .offset:         24
        .size:           8
        .value_kind:     global_buffer
      - .actual_access:  read_only
        .address_space:  global
        .offset:         32
        .size:           8
        .value_kind:     global_buffer
      - .actual_access:  write_only
        .address_space:  global
        .offset:         40
        .size:           8
        .value_kind:     global_buffer
      - .actual_access:  write_only
        .address_space:  global
        .offset:         48
        .size:           8
        .value_kind:     global_buffer
      - .address_space:  global
        .offset:         56
        .size:           8
        .value_kind:     global_buffer
      - .actual_access:  write_only
        .address_space:  global
        .offset:         64
        .size:           8
        .value_kind:     global_buffer
    .group_segment_fixed_size: 56768
    .kernarg_segment_align: 8
    .kernarg_segment_size: 72
    .language:       OpenCL C
    .language_version:
      - 2
      - 0
    .max_flat_workgroup_size: 768
    .name:           _Z5k3_vqPKDF16_S0_S0_S0_PKfPiPfS3_S4_
    .private_segment_fixed_size: 0
    .sgpr_count:     54
    .sgpr_spill_count: 0
    .symbol:         _Z5k3_vqPKDF16_S0_S0_S0_PKfPiPfS3_S4_.kd
    .uniform_work_group_size: 1
    .uses_dynamic_stack: false
    .vgpr_count:     72
    .vgpr_spill_count: 0
    .wavefront_size: 64
  - .agpr_count:     0
    .args:
      - .actual_access:  read_only
        .address_space:  global
        .offset:         0
        .size:           8
        .value_kind:     global_buffer
      - .actual_access:  read_only
        .address_space:  global
        .offset:         8
        .size:           8
        .value_kind:     global_buffer
      - .address_space:  global
        .offset:         16
        .size:           8
        .value_kind:     global_buffer
      - .actual_access:  read_only
        .address_space:  global
        .offset:         24
        .size:           8
        .value_kind:     global_buffer
      - .actual_access:  read_only
        .address_space:  global
        .offset:         32
        .size:           8
        .value_kind:     global_buffer
      - .actual_access:  read_only
        .address_space:  global
        .offset:         40
        .size:           8
        .value_kind:     global_buffer
      - .actual_access:  read_only
        .address_space:  global
        .offset:         48
        .size:           8
        .value_kind:     global_buffer
      - .actual_access:  read_only
        .address_space:  global
        .offset:         56
        .size:           8
        .value_kind:     global_buffer
      - .actual_access:  read_only
        .address_space:  global
        .offset:         64
        .size:           8
        .value_kind:     global_buffer
      - .actual_access:  read_only
        .address_space:  global
        .offset:         72
        .size:           8
        .value_kind:     global_buffer
      - .actual_access:  read_only
        .address_space:  global
        .offset:         80
        .size:           8
        .value_kind:     global_buffer
      - .address_space:  global
        .offset:         88
        .size:           8
        .value_kind:     global_buffer
      - .actual_access:  read_only
        .address_space:  global
        .offset:         96
        .size:           8
        .value_kind:     global_buffer
      - .actual_access:  read_only
        .address_space:  global
        .offset:         104
        .size:           8
        .value_kind:     global_buffer
      - .actual_access:  read_only
        .address_space:  global
        .offset:         112
        .size:           8
        .value_kind:     global_buffer
      - .actual_access:  read_only
        .address_space:  global
        .offset:         120
        .size:           8
        .value_kind:     global_buffer
      - .actual_access:  read_only
        .address_space:  global
        .offset:         128
        .size:           8
        .value_kind:     global_buffer
      - .address_space:  global
        .offset:         136
        .size:           8
        .value_kind:     global_buffer
      - .address_space:  global
        .offset:         144
        .size:           8
        .value_kind:     global_buffer
      - .actual_access:  write_only
        .address_space:  global
        .offset:         152
        .size:           8
        .value_kind:     global_buffer
      - .offset:         160
        .size:           4
        .value_kind:     hidden_block_count_x
      - .offset:         164
        .size:           4
        .value_kind:     hidden_block_count_y
      - .offset:         168
        .size:           4
        .value_kind:     hidden_block_count_z
      - .offset:         172
        .size:           2
        .value_kind:     hidden_group_size_x
      - .offset:         174
        .size:           2
        .value_kind:     hidden_group_size_y
      - .offset:         176
        .size:           2
        .value_kind:     hidden_group_size_z
      - .offset:         178
        .size:           2
        .value_kind:     hidden_remainder_x
      - .offset:         180
        .size:           2
        .value_kind:     hidden_remainder_y
      - .offset:         182
        .size:           2
        .value_kind:     hidden_remainder_z
      - .offset:         200
        .size:           8
        .value_kind:     hidden_global_offset_x
      - .offset:         208
        .size:           8
        .value_kind:     hidden_global_offset_y
      - .offset:         216
        .size:           8
        .value_kind:     hidden_global_offset_z
      - .offset:         224
        .size:           2
        .value_kind:     hidden_grid_dims
      - .offset:         280
        .size:           4
        .value_kind:     hidden_dynamic_lds_size
    .group_segment_fixed_size: 0
    .kernarg_segment_align: 8
    .kernarg_segment_size: 416
    .language:       OpenCL C
    .language_version:
      - 2
      - 0
    .max_flat_workgroup_size: 768
    .name:           _Z7k5_convPKDF16_PKiS0_PKfS4_S4_S4_S4_S4_S4_S4_PfS4_S4_S2_S2_S4_PiS5_S5_
    .private_segment_fixed_size: 0
    .sgpr_count:     51
    .sgpr_spill_count: 0
    .symbol:         _Z7k5_convPKDF16_PKiS0_PKfS4_S4_S4_S4_S4_S4_S4_PfS4_S4_S2_S2_S4_PiS5_S5_.kd
    .uniform_work_group_size: 1
    .uses_dynamic_stack: false
    .vgpr_count:     76
    .vgpr_spill_count: 0
    .wavefront_size: 64
